# rows<2>: rank values of all rows of a wave fetched once as lane-indexed vectors and broadcast with ds_bpermute, next row residual prefetched during the current row (two round trips per row instead of
# speedup vs baseline: 1.0048x; 1.0048x over previous
; DEVI float bflo(unsigned w) { return __uint_as_float(w << 16); }
; DEVI float bfhi(unsigned w) { return __uint_as_float(w & 0xffff0000u); }
; DEVI int obid() { int b = blockIdx.x; asm volatile("" : "+s"(b)); return b; }
; DEVI float wave_sum(float s) {
; #pragma unroll
;     for (int off = 32; off >= 1; off >>= 1) s += __shfl_xor(s, off);
;     return s;
; template <int MODE>
; DEVI void phase_rows(const Params& p, int l, char* smem) {
;     ...
;     for (int row = obid() * 8 + wid; row < nrows; row += gridDim.x * 8) {
;         const bool lat = row < NLAT;
;         const int b = lat ? (row >> 11) : ((row - NLAT) >> 8);
;         const int tok = lat ? (row & 2047) : (SEQ + ((row - NLAT) & 255));
;         float v[32];
;         if (MODE == 0) { const float* src = lat ? p.x + (size_t)row * DM : p.ctx + (size_t)(row - NLAT) * DM;
; #pragma unroll
;             for (int i = 0; i < 8; ++i) { const f32x4 t = *(const f32x4*)(src + i * 256 + lane * 4); v[i * 4] = t[0]; v[i * 4 + 1] = t[1]; v[i * 4 + 2] = t[2]; v[i * 4 + 3] = t[3]; }
;         } else { const bf16_t* src = xres + (size_t)row * DM;
; #pragma unroll
;             for (int i = 0; i < 8; ++i) { const u32x2 t = *(const u32x2*)(src + i * 256 + lane * 4); v[i * 4] = bflo(t[0]); v[i * 4 + 1] = bfhi(t[0]); v[i * 4 + 2] = bflo(t[1]); v[i * 4 + 3] = bfhi(t[1]); }
;         }
;         const float* mrow = mod + (size_t)(((MODE == 2) ? l : l) * 5 + (lat ? b : 4)) * 12288;
;         if (MODE == 2 || MODE == 3) {
;             float cacc[32];
; #pragma unroll
;             for (int i = 0; i < 32; ++i) cacc[i] = 0.f;
;             const int* rk = (const int*)(p.ws + WS_RANK) + (size_t)b * 16 * KEYS + tok;
;             const bf16_t* ydn = (const bf16_t*)(p.ws + WS_YDN);
;             const int cap = lat ? 256 : 32;
;             int rke[16];
; #pragma unroll
;             for (int e = 0; e < 16; ++e) rke[e] = rk[e * KEYS];
.LBB0_1677:
	s_and_b64 vcc, exec, s[14:15]
	s_cbranch_vccz .LBB0_2004
	v_readlane_b32 s4, v254, 36
	v_readlane_b32 s5, v254, 37
	s_and_b64 vcc, exec, s[4:5]
	s_cbranch_vccz .LBB0_2004
	v_mov_b32_e32 v1, v0
	s_mov_b32 s4, s2
	s_nop 0
	v_ashrrev_i32_e32 v2, 6, v1
	s_waitcnt vmcnt(0)
	v_lshl_add_u32 v36, s4, 3, v2
	s_movk_i32 s4, 0x2400
	v_cmp_gt_i32_e32 vcc, s4, v36
	s_and_saveexec_b64 s[14:15], vcc
	s_cbranch_execz .LBB0_1908
	v_lshlrev_b32_e32 v1, 2, v1
	v_and_b32_e32 v38, 0xfc, v1
	v_and_b32_e32 v1, 64, v227
	v_add_u32_e32 v1, 64, v1
	v_xor_b32_e32 v2, 32, v227
	v_cmp_lt_i32_e32 vcc, v2, v1
	s_load_dword s4, s[66:67], 0x0
	v_readlane_b32 s6, v253, 2
	v_cndmask_b32_e32 v2, v227, v2, vcc
	v_lshlrev_b32_e32 v39, 2, v2
	v_xor_b32_e32 v2, 16, v227
	v_cmp_lt_i32_e32 vcc, v2, v1
	v_readlane_b32 s7, v253, 3
	s_waitcnt lgkmcnt(0)
	s_lshl_b32 s44, s4, 3
	v_cndmask_b32_e32 v2, v227, v2, vcc
	v_lshlrev_b32_e32 v87, 2, v2
	v_xor_b32_e32 v2, 8, v227
	v_cmp_lt_i32_e32 vcc, v2, v1
	s_mov_b64 s[42:43], 0
	s_nop 0
	v_cndmask_b32_e32 v2, v227, v2, vcc
	v_lshlrev_b32_e32 v140, 2, v2
	v_xor_b32_e32 v2, 4, v227
	v_cmp_lt_i32_e32 vcc, v2, v1
	s_nop 1
	v_cndmask_b32_e32 v2, v227, v2, vcc
	v_lshlrev_b32_e32 v141, 2, v2
	v_xor_b32_e32 v2, 2, v227
	v_cmp_lt_i32_e32 vcc, v2, v1
	s_nop 1
	v_cndmask_b32_e32 v2, v227, v2, vcc
	v_lshlrev_b32_e32 v142, 2, v2
	v_xor_b32_e32 v2, 1, v227
	v_cmp_lt_i32_e32 vcc, v2, v1
	s_nop 1
	v_cndmask_b32_e32 v1, v227, v2, vcc
	v_lshlrev_b32_e32 v2, 1, v38
	v_lshlrev_b32_e32 v143, 2, v1
	v_lshl_add_u64 v[40:41], s[6:7], 0, v[2:3]
	v_lshl_add_u64 v[42:43], s[26:27], 0, v[2:3]
	v_readlane_b32 s4, v254, 22
	v_readlane_b32 s5, v254, 23
	v_mov_b32_e32 v203, 0
	v_mov_b32_e32 v204, 4
	v_mov_b32_e32 v205, 8
	v_mov_b32_e32 v206, 12
	v_mov_b32_e32 v207, 16
	v_mov_b32_e32 v208, 20
	v_mov_b32_e32 v209, 24
	v_mov_b32_e32 v210, 28
	v_mov_b32_e32 v211, 32
	v_mov_b32_e32 v212, 36
	v_mov_b32_e32 v213, 40
	v_mov_b32_e32 v214, 44
	v_mov_b32_e32 v215, 48
	v_mov_b32_e32 v216, 52
	v_mov_b32_e32 v217, 56
	v_mov_b32_e32 v218, 60
	v_and_b32_e32 v219, 15, v0
	v_mul_u32_u24_e32 v219, 0x2400, v219
	v_lshl_add_u32 v220, v36, 2, v219
	global_load_dword v198, v220, s[4:5]
	v_add_u32_e32 v221, 0x24000, v220
	global_load_dword v199, v221, s[4:5]
	v_add_u32_e32 v180, 0x48000, v220
	global_load_dword v200, v180, s[4:5]
	v_add_u32_e32 v183, 0x6c000, v220
	global_load_dword v201, v183, s[4:5]
	v_lshrrev_b32_e32 v184, 8, v36
	v_mul_u32_u24_e32 v184, 0x24000, v184
	v_and_b32_e32 v187, 0xff, v36
	v_or_b32_e32 v187, 0x800, v187
	v_lshl_add_u32 v184, v187, 2, v184
	v_add_u32_e32 v184, v184, v219
	global_load_dword v202, v184, s[4:5]
	v_lshlrev_b32_e32 v248, 12, v36
	v_mov_b32_e32 v249, 0
	v_lshl_add_u64 v[248:249], v[42:43], 0, v[248:249]
	global_load_dwordx2 v[176:177], v[248:249], off
	global_load_dwordx2 v[178:179], v[248:249], off offset:512
	global_load_dwordx2 v[228:229], v[248:249], off offset:1024
	global_load_dwordx2 v[232:233], v[248:249], off offset:1536
	global_load_dwordx2 v[236:237], v[248:249], off offset:2048
	global_load_dwordx2 v[240:241], v[248:249], off offset:2560
	global_load_dwordx2 v[242:243], v[248:249], off offset:3072
	global_load_dwordx2 v[246:247], v[248:249], off offset:3584
	s_waitcnt vmcnt(0)
	s_branch .LBB0_1684

; DEVI float bflo(unsigned w) { return __uint_as_float(w << 16); }
; DEVI float bfhi(unsigned w) { return __uint_as_float(w & 0xffff0000u); }
; template <int MODE>
; DEVI void phase_rows(const Params& p, int l, char* smem) {
;     ...
;             {   u32x2 w0[8], w1[8], w2[8], w3[8];
; #pragma unroll
;                 for (int i = 0; i < 8; ++i) { w0[i] = *(const u32x2*)(y0 + i * 256 + lane * 4); w1[i] = *(const u32x2*)(y1 + i * 256 + lane * 4);
;                     w2[i] = *(const u32x2*)(y2 + i * 256 + lane * 4); w3[i] = *(const u32x2*)(y3 + i * 256 + lane * 4); }
;                 const float f0 = ny > 0 ? 1.f : 0.f, f1 = ny > 1 ? 1.f : 0.f, f2 = ny > 2 ? 1.f : 0.f, f3 = ny > 3 ? 1.f : 0.f;
; #pragma unroll
;                 for (int i = 0; i < 8; ++i) {
;                     cacc[i * 4] += f0 * bflo(w0[i][0]) + f1 * bflo(w1[i][0]) + f2 * bflo(w2[i][0]) + f3 * bflo(w3[i][0]);
;                     cacc[i * 4 + 1] += f0 * bfhi(w0[i][0]) + f1 * bfhi(w1[i][0]) + f2 * bfhi(w2[i][0]) + f3 * bfhi(w3[i][0]);
;                     cacc[i * 4 + 2] += f0 * bflo(w0[i][1]) + f1 * bflo(w1[i][1]) + f2 * bflo(w2[i][1]) + f3 * bflo(w3[i][1]);
;                     cacc[i * 4 + 3] += f0 * bfhi(w0[i][1]) + f1 * bfhi(w1[i][1]) + f2 * bfhi(w2[i][1]) + f3 * bfhi(w3[i][1]); }
;             }
;             const float* gf = mrow + 10240;
; #pragma unroll
;             for (int i = 0; i < 8; ++i) { const f32x4 g = *(const f32x4*)(gf + i * 256 + lane * 4);
;                 v[i * 4] += g[0] * cacc[i * 4]; v[i * 4 + 1] += g[1] * cacc[i * 4 + 1]; v[i * 4 + 2] += g[2] * cacc[i * 4 + 2]; v[i * 4 + 3] += g[3] * cacc[i * 4 + 3]; }
.LBB0_1683:
	s_or_b64 exec, exec, s[16:17]
	v_lshlrev_b32_e32 v2, 1, v38
	v_lshl_add_u64 v[66:67], v[66:67], 0, v[2:3]
	v_lshlrev_b32_e32 v120, 16, v64
	v_and_b32_e32 v121, 0xffff0000, v64
	v_lshlrev_b32_e32 v122, 16, v65
	v_and_b32_e32 v123, 0xffff0000, v65
	v_lshl_add_u64 v[64:65], v[72:73], 0, v[2:3]
	global_load_dwordx2 v[156:157], v[66:67], off
	global_load_dwordx2 v[158:159], v[64:65], off
	v_lshl_add_u64 v[68:69], v[68:69], 0, v[2:3]
	global_load_dwordx2 v[160:161], v[68:69], off
	v_lshl_add_u64 v[70:71], v[70:71], 0, v[2:3]
	global_load_dwordx2 v[132:133], v[70:71], off
	v_readlane_b32 s4, v254, 18
	v_readlane_b32 s5, v254, 19
	v_lshlrev_b32_e32 v2, 2, v38
	v_lshlrev_b32_e32 v116, 16, v62
	v_lshl_add_u64 v[50:51], v[50:51], 2, s[4:5]
	v_lshl_add_u64 v[50:51], v[50:51], 0, v[2:3]
	s_mov_b32 s4, 0xb000
	v_add_co_u32_e32 v72, vcc, s4, v50
	s_mov_b64 s[4:5], 0xa000
	s_nop 0
	v_addc_co_u32_e32 v73, vcc, 0, v51, vcc
	global_load_dwordx4 v[144:147], v[72:73], off offset:-4096
	global_load_dwordx2 v[162:163], v[66:67], off offset:512
	global_load_dwordx2 v[164:165], v[64:65], off offset:512
	global_load_dwordx2 v[166:167], v[68:69], off offset:512
	global_load_dwordx2 v[130:131], v[70:71], off offset:512
	v_lshl_add_u64 v[168:169], v[50:51], 0, s[4:5]
	global_load_dwordx4 v[148:151], v[168:169], off offset:1024
	global_load_dwordx2 v[134:135], v[64:65], off offset:1024
	global_load_dwordx2 v[124:125], v[64:65], off offset:1536
	global_load_dwordx2 v[136:137], v[66:67], off offset:1024
	global_load_dwordx2 v[126:127], v[66:67], off offset:1536
	global_load_dwordx2 v[138:139], v[68:69], off offset:1024
	global_load_dwordx2 v[112:113], v[68:69], off offset:1536
	global_load_dwordx2 v[128:129], v[70:71], off offset:1024
	global_load_dwordx2 v[114:115], v[70:71], off offset:1536
	global_load_dwordx2 v[106:107], v[64:65], off offset:2048
	global_load_dwordx2 v[90:91], v[64:65], off offset:2560
	global_load_dwordx2 v[78:79], v[64:65], off offset:3072
	s_nop 0
	global_load_dwordx2 v[64:65], v[64:65], off offset:3584
	s_nop 0
	global_load_dwordx2 v[108:109], v[66:67], off offset:2048
	global_load_dwordx2 v[92:93], v[66:67], off offset:2560
	global_load_dwordx2 v[80:81], v[66:67], off offset:3072
	s_nop 0
	global_load_dwordx2 v[66:67], v[66:67], off offset:3584
	s_nop 0
	global_load_dwordx2 v[100:101], v[68:69], off offset:2048
	global_load_dwordx2 v[94:95], v[68:69], off offset:2560
	global_load_dwordx2 v[82:83], v[68:69], off offset:3072
	s_nop 0
	global_load_dwordx2 v[68:69], v[68:69], off offset:3584
	s_nop 0
	global_load_dwordx2 v[102:103], v[70:71], off offset:2048
	global_load_dwordx2 v[96:97], v[70:71], off offset:2560
	global_load_dwordx2 v[84:85], v[70:71], off offset:3072
	s_nop 0
	global_load_dwordx2 v[70:71], v[70:71], off offset:3584
	s_nop 0
	global_load_dwordx4 v[152:155], v[168:169], off offset:2048
	v_cmp_lt_u32_e32 vcc, 2, v88
	v_and_b32_e32 v117, 0xffff0000, v62
	v_lshlrev_b32_e32 v118, 16, v63
	v_cndmask_b32_e64 v2, 0, 1.0, vcc
	v_cmp_lt_u32_e32 vcc, 3, v88
	v_and_b32_e32 v119, 0xffff0000, v63
	v_lshlrev_b32_e32 v110, 16, v60
	v_cndmask_b32_e64 v86, 0, 1.0, vcc
	v_cmp_eq_u32_e32 vcc, 0, v88
	v_and_b32_e32 v111, 0xffff0000, v60
	v_lshlrev_b32_e32 v104, 16, v61
	v_cndmask_b32_e64 v89, 1.0, 0, vcc
	v_cmp_lt_u32_e32 vcc, 1, v88
	v_and_b32_e32 v105, 0xffff0000, v61
	v_lshlrev_b32_e32 v98, 16, v58
	v_cndmask_b32_e64 v88, 0, 1.0, vcc
	v_and_b32_e32 v99, 0xffff0000, v58
	v_lshlrev_b32_e32 v76, 16, v59
	v_and_b32_e32 v77, 0xffff0000, v59
	v_lshlrev_b32_e32 v74, 16, v56
	v_and_b32_e32 v75, 0xffff0000, v56
	v_lshlrev_b32_e32 v56, 16, v57
	v_and_b32_e32 v57, 0xffff0000, v57
	v_lshlrev_b32_e32 v60, 16, v54
	v_and_b32_e32 v61, 0xffff0000, v54
	v_lshlrev_b32_e32 v58, 16, v55
	v_and_b32_e32 v59, 0xffff0000, v55
	v_lshlrev_b32_e32 v54, 16, v52
	v_and_b32_e32 v55, 0xffff0000, v52
	v_lshlrev_b32_e32 v52, 16, v53
	v_and_b32_e32 v53, 0xffff0000, v53
	v_lshlrev_b32_e32 v62, 16, v48
	v_and_b32_e32 v63, 0xffff0000, v48
	v_lshlrev_b32_e32 v48, 16, v49
	v_and_b32_e32 v49, 0xffff0000, v49
	s_mov_b64 s[4:5], 0x3c000
	v_add_u32_e32 v36, s44, v36
	s_waitcnt vmcnt(34)
	v_and_b32_e32 v173, 0xffff0000, v157
	s_waitcnt vmcnt(33)
	v_lshlrev_b32_e32 v172, 16, v159
	v_lshlrev_b32_e32 v170, 16, v157
	v_and_b32_e32 v171, 0xffff0000, v159
	v_pk_mul_f32 v[172:173], v[88:89], v[172:173] op_sel:[1,0] op_sel_hi:[0,1]
	v_pk_fma_f32 v[170:171], v[88:89], v[170:171], v[172:173]
	s_waitcnt vmcnt(32)
	v_lshlrev_b32_e32 v172, 16, v161
	v_and_b32_e32 v173, 0xffff0000, v161
	v_pk_fma_f32 v[170:171], v[2:3], v[172:173], v[170:171] op_sel_hi:[0,1,1]
	s_waitcnt vmcnt(31)
	v_lshlrev_b32_e32 v172, 16, v133
	v_and_b32_e32 v173, 0xffff0000, v133
	v_pk_fma_f32 v[170:171], v[86:87], v[172:173], v[170:171] op_sel_hi:[0,1,1]
	v_pk_add_f32 v[170:171], v[6:7], v[170:171]
	v_lshlrev_b32_e32 v6, 16, v156
	v_and_b32_e32 v7, 0xffff0000, v158
	v_lshlrev_b32_e32 v172, 16, v158
	v_and_b32_e32 v173, 0xffff0000, v156
	global_load_dwordx4 v[156:159], v[168:169], off offset:3072
	v_lshlrev_b32_e32 v174, 16, v160
	v_and_b32_e32 v175, 0xffff0000, v160
	v_lshlrev_b32_e32 v160, 16, v132
	v_and_b32_e32 v161, 0xffff0000, v132
	v_pk_mul_f32 v[132:133], v[88:89], v[172:173] op_sel:[1,0] op_sel_hi:[0,1]
	v_pk_fma_f32 v[6:7], v[88:89], v[6:7], v[132:133]
	s_waitcnt vmcnt(28)
	v_lshlrev_b32_e32 v132, 16, v166
	v_pk_fma_f32 v[6:7], v[2:3], v[174:175], v[6:7] op_sel_hi:[0,1,1]
	v_pk_fma_f32 v[6:7], v[86:87], v[160:161], v[6:7] op_sel_hi:[0,1,1]
	v_pk_add_f32 v[4:5], v[4:5], v[6:7]
	v_and_b32_e32 v133, 0xffff0000, v166
	v_pk_fma_f32 v[6:7], v[4:5], v[144:145], v[120:121]
	v_pk_fma_f32 v[4:5], v[170:171], v[146:147], v[122:123]
	v_lshlrev_b32_e32 v122, 16, v164
	v_and_b32_e32 v123, 0xffff0000, v162
	v_lshlrev_b32_e32 v120, 16, v162
	v_and_b32_e32 v121, 0xffff0000, v164
	v_pk_mul_f32 v[122:123], v[88:89], v[122:123] op_sel:[1,0] op_sel_hi:[0,1]
	v_pk_fma_f32 v[120:121], v[88:89], v[120:121], v[122:123]
	s_waitcnt vmcnt(27)
; DEVI float bflo(unsigned w) { return __uint_as_float(w << 16); }
; DEVI float bfhi(unsigned w) { return __uint_as_float(w & 0xffff0000u); }
; template <int MODE>
; DEVI void phase_rows(const Params& p, int l, char* smem) {
;     ...
;                 for (int i = 0; i < 8; ++i) { w0[i] = *(const u32x2*)(y0 + i * 256 + lane * 4); w1[i] = *(const u32x2*)(y1 + i * 256 + lane * 4);
;                     w2[i] = *(const u32x2*)(y2 + i * 256 + lane * 4); w3[i] = *(const u32x2*)(y3 + i * 256 + lane * 4); }
;                 const float f0 = ny > 0 ? 1.f : 0.f, f1 = ny > 1 ? 1.f : 0.f, f2 = ny > 2 ? 1.f : 0.f, f3 = ny > 3 ? 1.f : 0.f;
; #pragma unroll
;                 for (int i = 0; i < 8; ++i) {
;                     cacc[i * 4] += f0 * bflo(w0[i][0]) + f1 * bflo(w1[i][0]) + f2 * bflo(w2[i][0]) + f3 * bflo(w3[i][0]);
;                     cacc[i * 4 + 1] += f0 * bfhi(w0[i][0]) + f1 * bfhi(w1[i][0]) + f2 * bfhi(w2[i][0]) + f3 * bfhi(w3[i][0]);
;                     cacc[i * 4 + 2] += f0 * bflo(w0[i][1]) + f1 * bflo(w1[i][1]) + f2 * bflo(w2[i][1]) + f3 * bflo(w3[i][1]);
;                     cacc[i * 4 + 3] += f0 * bfhi(w0[i][1]) + f1 * bfhi(w1[i][1]) + f2 * bfhi(w2[i][1]) + f3 * bfhi(w3[i][1]); }
;             }
;             const float* gf = mrow + 10240;
; #pragma unroll
;             for (int i = 0; i < 8; ++i) { const f32x4 g = *(const f32x4*)(gf + i * 256 + lane * 4);
;                 v[i * 4] += g[0] * cacc[i * 4]; v[i * 4 + 1] += g[1] * cacc[i * 4 + 1]; v[i * 4 + 2] += g[2] * cacc[i * 4 + 2]; v[i * 4 + 3] += g[3] * cacc[i * 4 + 3]; }
	v_lshlrev_b32_e32 v144, 16, v130
	v_and_b32_e32 v145, 0xffff0000, v130
	v_pk_fma_f32 v[120:121], v[2:3], v[132:133], v[120:121] op_sel_hi:[0,1,1]
	v_pk_fma_f32 v[120:121], v[86:87], v[144:145], v[120:121] op_sel_hi:[0,1,1]
	v_pk_add_f32 v[8:9], v[8:9], v[120:121]
	global_load_dwordx4 v[120:123], v[72:73], off
	v_lshlrev_b32_e32 v132, 16, v165
	v_and_b32_e32 v133, 0xffff0000, v163
	s_waitcnt vmcnt(27)
	v_pk_fma_f32 v[8:9], v[8:9], v[148:149], v[116:117]
	v_lshlrev_b32_e32 v116, 16, v163
	v_and_b32_e32 v117, 0xffff0000, v165
	v_pk_mul_f32 v[132:133], v[88:89], v[132:133] op_sel:[1,0] op_sel_hi:[0,1]
	v_lshlrev_b32_e32 v144, 16, v167
	v_and_b32_e32 v145, 0xffff0000, v167
	v_pk_fma_f32 v[116:117], v[88:89], v[116:117], v[132:133]
	v_lshlrev_b32_e32 v130, 16, v131
	v_and_b32_e32 v131, 0xffff0000, v131
	v_pk_fma_f32 v[116:117], v[2:3], v[144:145], v[116:117] op_sel_hi:[0,1,1]
	v_pk_fma_f32 v[116:117], v[86:87], v[130:131], v[116:117] op_sel_hi:[0,1,1]
	v_pk_add_f32 v[10:11], v[10:11], v[116:117]
	s_waitcnt vmcnt(24)
	v_lshlrev_b32_e32 v116, 16, v136
	v_pk_fma_f32 v[10:11], v[10:11], v[150:151], v[118:119]
	v_lshlrev_b32_e32 v118, 16, v134
	v_and_b32_e32 v119, 0xffff0000, v136
	v_and_b32_e32 v117, 0xffff0000, v134
	v_pk_mul_f32 v[118:119], v[88:89], v[118:119] op_sel:[1,0] op_sel_hi:[0,1]
	s_waitcnt vmcnt(22)
	v_lshlrev_b32_e32 v130, 16, v138
	v_and_b32_e32 v131, 0xffff0000, v138
	v_pk_fma_f32 v[116:117], v[88:89], v[116:117], v[118:119]
	s_waitcnt vmcnt(20)
	v_lshlrev_b32_e32 v132, 16, v128
	v_and_b32_e32 v133, 0xffff0000, v128
	v_pk_fma_f32 v[116:117], v[2:3], v[130:131], v[116:117] op_sel_hi:[0,1,1]
	v_pk_fma_f32 v[116:117], v[86:87], v[132:133], v[116:117] op_sel_hi:[0,1,1]
	v_pk_add_f32 v[12:13], v[12:13], v[116:117]
	global_load_dwordx4 v[116:119], v[72:73], off offset:1024
	v_lshlrev_b32_e32 v130, 16, v135
	v_and_b32_e32 v131, 0xffff0000, v137
	s_waitcnt vmcnt(3)
	v_pk_fma_f32 v[12:13], v[12:13], v[152:153], v[110:111]
	v_lshlrev_b32_e32 v110, 16, v137
	v_and_b32_e32 v111, 0xffff0000, v135
	v_pk_mul_f32 v[130:131], v[88:89], v[130:131] op_sel:[1,0] op_sel_hi:[0,1]
	v_lshlrev_b32_e32 v132, 16, v139
	v_and_b32_e32 v133, 0xffff0000, v139
	v_pk_fma_f32 v[110:111], v[88:89], v[110:111], v[130:131]
	v_lshlrev_b32_e32 v128, 16, v129
	v_and_b32_e32 v129, 0xffff0000, v129
	v_pk_fma_f32 v[110:111], v[2:3], v[132:133], v[110:111] op_sel_hi:[0,1,1]
	v_pk_fma_f32 v[110:111], v[86:87], v[128:129], v[110:111] op_sel_hi:[0,1,1]
	v_pk_add_f32 v[14:15], v[14:15], v[110:111]
	v_lshlrev_b32_e32 v110, 16, v124
	v_and_b32_e32 v111, 0xffff0000, v126
	v_pk_fma_f32 v[14:15], v[14:15], v[154:155], v[104:105]
	v_lshlrev_b32_e32 v104, 16, v126
	v_and_b32_e32 v105, 0xffff0000, v124
	v_pk_mul_f32 v[110:111], v[88:89], v[110:111] op_sel:[1,0] op_sel_hi:[0,1]
	v_lshlrev_b32_e32 v128, 16, v112
	v_and_b32_e32 v129, 0xffff0000, v112
	v_pk_fma_f32 v[104:105], v[88:89], v[104:105], v[110:111]
	v_lshlrev_b32_e32 v130, 16, v114
	v_and_b32_e32 v131, 0xffff0000, v114
	v_pk_fma_f32 v[104:105], v[2:3], v[128:129], v[104:105] op_sel_hi:[0,1,1]
	v_pk_fma_f32 v[104:105], v[86:87], v[130:131], v[104:105] op_sel_hi:[0,1,1]
	v_pk_add_f32 v[16:17], v[16:17], v[104:105]
	v_lshlrev_b32_e32 v104, 16, v125
	s_waitcnt vmcnt(2)
	v_pk_fma_f32 v[16:17], v[16:17], v[156:157], v[98:99]
	v_lshlrev_b32_e32 v98, 16, v127
	v_and_b32_e32 v99, 0xffff0000, v125
	v_and_b32_e32 v105, 0xffff0000, v127
	global_load_dwordx4 v[124:127], v[72:73], off offset:2048
	v_pk_mul_f32 v[104:105], v[88:89], v[104:105] op_sel:[1,0] op_sel_hi:[0,1]
	v_lshlrev_b32_e32 v110, 16, v113
	v_and_b32_e32 v111, 0xffff0000, v113
	v_pk_fma_f32 v[98:99], v[88:89], v[98:99], v[104:105]
	v_lshlrev_b32_e32 v112, 16, v115
	v_and_b32_e32 v113, 0xffff0000, v115
	v_pk_fma_f32 v[98:99], v[2:3], v[110:111], v[98:99] op_sel_hi:[0,1,1]
	v_pk_fma_f32 v[98:99], v[86:87], v[112:113], v[98:99] op_sel_hi:[0,1,1]
	v_pk_add_f32 v[18:19], v[18:19], v[98:99]
	v_lshlrev_b32_e32 v98, 16, v106
	v_and_b32_e32 v99, 0xffff0000, v108
	v_pk_fma_f32 v[18:19], v[18:19], v[158:159], v[76:77]
	v_lshlrev_b32_e32 v76, 16, v108
	v_and_b32_e32 v77, 0xffff0000, v106
	v_pk_mul_f32 v[98:99], v[88:89], v[98:99] op_sel:[1,0] op_sel_hi:[0,1]
	v_lshlrev_b32_e32 v104, 16, v100
	v_and_b32_e32 v105, 0xffff0000, v100
	v_pk_fma_f32 v[76:77], v[88:89], v[76:77], v[98:99]
	v_lshlrev_b32_e32 v110, 16, v102
	v_and_b32_e32 v111, 0xffff0000, v102
	v_pk_fma_f32 v[76:77], v[2:3], v[104:105], v[76:77] op_sel_hi:[0,1,1]
	v_pk_fma_f32 v[76:77], v[86:87], v[110:111], v[76:77] op_sel_hi:[0,1,1]
	v_pk_add_f32 v[20:21], v[20:21], v[76:77]
	v_lshlrev_b32_e32 v98, 16, v107
	s_waitcnt vmcnt(2)
	v_pk_fma_f32 v[20:21], v[20:21], v[120:121], v[74:75]
	global_load_dwordx4 v[72:75], v[72:73], off offset:3072
	v_and_b32_e32 v99, 0xffff0000, v109
	v_lshlrev_b32_e32 v76, 16, v109
	v_and_b32_e32 v77, 0xffff0000, v107
	v_pk_mul_f32 v[98:99], v[88:89], v[98:99] op_sel:[1,0] op_sel_hi:[0,1]
	v_lshlrev_b32_e32 v100, 16, v101
	v_and_b32_e32 v101, 0xffff0000, v101
	v_pk_fma_f32 v[76:77], v[88:89], v[76:77], v[98:99]
	v_lshlrev_b32_e32 v102, 16, v103
	v_and_b32_e32 v103, 0xffff0000, v103
	v_pk_fma_f32 v[76:77], v[2:3], v[100:101], v[76:77] op_sel_hi:[0,1,1]
	v_pk_fma_f32 v[76:77], v[86:87], v[102:103], v[76:77] op_sel_hi:[0,1,1]
	v_pk_add_f32 v[22:23], v[22:23], v[76:77]
	v_lshlrev_b32_e32 v76, 16, v90
	v_and_b32_e32 v77, 0xffff0000, v92
	v_pk_fma_f32 v[22:23], v[22:23], v[122:123], v[56:57]
	v_lshlrev_b32_e32 v56, 16, v92
	v_and_b32_e32 v57, 0xffff0000, v90
	v_pk_mul_f32 v[76:77], v[88:89], v[76:77] op_sel:[1,0] op_sel_hi:[0,1]
	v_lshlrev_b32_e32 v98, 16, v94
	v_and_b32_e32 v99, 0xffff0000, v94
	v_pk_fma_f32 v[56:57], v[88:89], v[56:57], v[76:77]
	v_lshlrev_b32_e32 v100, 16, v96
	v_and_b32_e32 v101, 0xffff0000, v96
	v_pk_fma_f32 v[56:57], v[2:3], v[98:99], v[56:57] op_sel_hi:[0,1,1]
	v_pk_fma_f32 v[56:57], v[86:87], v[100:101], v[56:57] op_sel_hi:[0,1,1]
	v_pk_add_f32 v[24:25], v[24:25], v[56:57]
	v_lshlrev_b32_e32 v56, 16, v93
	s_waitcnt vmcnt(2)
; DEVI unsigned cvt_pk(float lo, float hi) { f32x2 v = {lo, hi}; bf16x2_t b = __builtin_convertvector(v, bf16x2_t); return __builtin_bit_cast(unsigned, b); }
; DEVI float bflo(unsigned w) { return __uint_as_float(w << 16); }
; DEVI float bfhi(unsigned w) { return __uint_as_float(w & 0xffff0000u); }
; template <int MODE>
; DEVI void phase_rows(const Params& p, int l, char* smem) {
;     ...
;                 for (int i = 0; i < 8; ++i) {
;                     cacc[i * 4] += f0 * bflo(w0[i][0]) + f1 * bflo(w1[i][0]) + f2 * bflo(w2[i][0]) + f3 * bflo(w3[i][0]);
;                     cacc[i * 4 + 1] += f0 * bfhi(w0[i][0]) + f1 * bfhi(w1[i][0]) + f2 * bfhi(w2[i][0]) + f3 * bfhi(w3[i][0]);
;                     cacc[i * 4 + 2] += f0 * bflo(w0[i][1]) + f1 * bflo(w1[i][1]) + f2 * bflo(w2[i][1]) + f3 * bflo(w3[i][1]);
;                     cacc[i * 4 + 3] += f0 * bfhi(w0[i][1]) + f1 * bfhi(w1[i][1]) + f2 * bfhi(w2[i][1]) + f3 * bfhi(w3[i][1]); }
;             }
;             const float* gf = mrow + 10240;
; #pragma unroll
;             for (int i = 0; i < 8; ++i) { const f32x4 g = *(const f32x4*)(gf + i * 256 + lane * 4);
;                 v[i * 4] += g[0] * cacc[i * 4]; v[i * 4 + 1] += g[1] * cacc[i * 4 + 1]; v[i * 4 + 2] += g[2] * cacc[i * 4 + 2]; v[i * 4 + 3] += g[3] * cacc[i * 4 + 3]; }
;             if (MODE == 2) {
; #pragma unroll
;                 for (int i = 0; i < 8; ++i) *(u32x2*)(xres + (size_t)row * DM + i * 256 + lane * 4) = (u32x2){cvt_pk(v[i * 4], v[i * 4 + 1]), cvt_pk(v[i * 4 + 2], v[i * 4 + 3])};
;             }
;         }
;         f32x4 shv[8], scv[8];
;         if (MODE != 3) { const float* mr2 = (MODE == 2) ? mrow + (size_t)5 * 12288 : mrow;
;             const float* sh = mr2 + ((MODE == 1) ? 6144 : 0); const float* sc = mr2 + ((MODE == 1) ? 8192 : 2048);
; #pragma unroll
;             for (int i = 0; i < 8; ++i) { shv[i] = *(const f32x4*)(sh + i * 256 + lane * 4); scv[i] = *(const f32x4*)(sc + i * 256 + lane * 4); } }
;         float ss = 0.f;
; #pragma unroll
;         for (int i = 0; i < 32; ++i) ss += v[i] * v[i];
	v_pk_fma_f32 v[24:25], v[24:25], v[116:117], v[60:61]
	v_lshlrev_b32_e32 v60, 16, v91
	v_and_b32_e32 v61, 0xffff0000, v93
	v_and_b32_e32 v57, 0xffff0000, v91
	v_pk_mul_f32 v[60:61], v[88:89], v[60:61] op_sel:[1,0] op_sel_hi:[0,1]
	v_lshlrev_b32_e32 v76, 16, v95
	v_and_b32_e32 v77, 0xffff0000, v95
	v_pk_fma_f32 v[56:57], v[88:89], v[56:57], v[60:61]
	v_lshlrev_b32_e32 v90, 16, v97
	v_and_b32_e32 v91, 0xffff0000, v97
	v_pk_fma_f32 v[56:57], v[2:3], v[76:77], v[56:57] op_sel_hi:[0,1,1]
	v_pk_fma_f32 v[56:57], v[86:87], v[90:91], v[56:57] op_sel_hi:[0,1,1]
	v_pk_add_f32 v[26:27], v[26:27], v[56:57]
	v_lshlrev_b32_e32 v56, 16, v80
	v_pk_fma_f32 v[26:27], v[26:27], v[118:119], v[58:59]
	v_lshlrev_b32_e32 v58, 16, v78
	v_and_b32_e32 v59, 0xffff0000, v80
	v_and_b32_e32 v57, 0xffff0000, v78
	v_pk_mul_f32 v[58:59], v[88:89], v[58:59] op_sel:[1,0] op_sel_hi:[0,1]
	v_lshlrev_b32_e32 v60, 16, v82
	v_and_b32_e32 v61, 0xffff0000, v82
	v_pk_fma_f32 v[56:57], v[88:89], v[56:57], v[58:59]
	v_lshlrev_b32_e32 v76, 16, v84
	v_and_b32_e32 v77, 0xffff0000, v84
	v_pk_fma_f32 v[56:57], v[2:3], v[60:61], v[56:57] op_sel_hi:[0,1,1]
	v_pk_fma_f32 v[56:57], v[86:87], v[76:77], v[56:57] op_sel_hi:[0,1,1]
	v_pk_add_f32 v[28:29], v[28:29], v[56:57]
	v_lshlrev_b32_e32 v56, 16, v79
	v_and_b32_e32 v57, 0xffff0000, v81
	s_waitcnt vmcnt(1)
	v_pk_fma_f32 v[28:29], v[28:29], v[124:125], v[54:55]
	v_lshlrev_b32_e32 v54, 16, v81
	v_and_b32_e32 v55, 0xffff0000, v79
	v_pk_mul_f32 v[56:57], v[88:89], v[56:57] op_sel:[1,0] op_sel_hi:[0,1]
	v_lshlrev_b32_e32 v58, 16, v83
	v_and_b32_e32 v59, 0xffff0000, v83
	v_pk_fma_f32 v[54:55], v[88:89], v[54:55], v[56:57]
	v_lshlrev_b32_e32 v60, 16, v85
	v_and_b32_e32 v61, 0xffff0000, v85
	v_pk_fma_f32 v[54:55], v[2:3], v[58:59], v[54:55] op_sel_hi:[0,1,1]
	v_pk_fma_f32 v[54:55], v[86:87], v[60:61], v[54:55] op_sel_hi:[0,1,1]
	v_pk_add_f32 v[30:31], v[30:31], v[54:55]
	v_lshlrev_b32_e32 v54, 16, v64
	v_and_b32_e32 v55, 0xffff0000, v66
	v_pk_fma_f32 v[30:31], v[30:31], v[126:127], v[52:53]
	v_lshlrev_b32_e32 v52, 16, v66
	v_and_b32_e32 v53, 0xffff0000, v64
	v_pk_mul_f32 v[54:55], v[88:89], v[54:55] op_sel:[1,0] op_sel_hi:[0,1]
	v_lshlrev_b32_e32 v56, 16, v68
	v_and_b32_e32 v57, 0xffff0000, v68
	v_pk_fma_f32 v[52:53], v[88:89], v[52:53], v[54:55]
	v_lshlrev_b32_e32 v58, 16, v70
	v_and_b32_e32 v59, 0xffff0000, v70
	v_pk_fma_f32 v[52:53], v[2:3], v[56:57], v[52:53] op_sel_hi:[0,1,1]
	v_pk_fma_f32 v[52:53], v[86:87], v[58:59], v[52:53] op_sel_hi:[0,1,1]
	v_lshlrev_b32_e32 v54, 16, v65
	v_and_b32_e32 v55, 0xffff0000, v67
	v_pk_add_f32 v[32:33], v[32:33], v[52:53]
	v_lshlrev_b32_e32 v52, 16, v67
	v_and_b32_e32 v53, 0xffff0000, v65
	v_pk_mul_f32 v[54:55], v[88:89], v[54:55] op_sel:[1,0] op_sel_hi:[0,1]
	v_lshlrev_b32_e32 v56, 16, v69
	v_and_b32_e32 v57, 0xffff0000, v69
	v_pk_fma_f32 v[52:53], v[88:89], v[52:53], v[54:55]
	v_lshlrev_b32_e32 v58, 16, v71
	v_and_b32_e32 v59, 0xffff0000, v71
	v_pk_fma_f32 v[52:53], v[2:3], v[56:57], v[52:53] op_sel_hi:[0,1,1]
	v_pk_fma_f32 v[52:53], v[86:87], v[58:59], v[52:53] op_sel_hi:[0,1,1]
	v_pk_add_f32 v[34:35], v[34:35], v[52:53]
	s_waitcnt vmcnt(0)
	v_pk_fma_f32 v[32:33], v[32:33], v[72:73], v[62:63]
	v_pk_fma_f32 v[34:35], v[34:35], v[74:75], v[48:49]
	v_cvt_pk_bf16_f32 v48, v6, v7
	v_cvt_pk_bf16_f32 v49, v4, v5
	global_store_dwordx2 v[44:45], v[48:49], off
	v_cvt_pk_bf16_f32 v48, v8, v9
	v_cvt_pk_bf16_f32 v49, v10, v11
	global_store_dwordx2 v[44:45], v[48:49], off offset:512
	v_cvt_pk_bf16_f32 v48, v12, v13
	v_cvt_pk_bf16_f32 v49, v14, v15
	global_store_dwordx2 v[44:45], v[48:49], off offset:1024
	v_cvt_pk_bf16_f32 v48, v16, v17
	v_cvt_pk_bf16_f32 v49, v18, v19
	global_store_dwordx2 v[44:45], v[48:49], off offset:1536
	v_cvt_pk_bf16_f32 v48, v20, v21
	v_cvt_pk_bf16_f32 v49, v22, v23
	global_store_dwordx2 v[44:45], v[48:49], off offset:2048
	v_cvt_pk_bf16_f32 v48, v24, v25
	v_cvt_pk_bf16_f32 v49, v26, v27
	global_store_dwordx2 v[44:45], v[48:49], off offset:2560
	v_cvt_pk_bf16_f32 v48, v28, v29
	v_cvt_pk_bf16_f32 v49, v30, v31
	global_store_dwordx2 v[44:45], v[48:49], off offset:3072
	v_cvt_pk_bf16_f32 v48, v32, v33
	v_cvt_pk_bf16_f32 v49, v34, v35
	global_store_dwordx2 v[44:45], v[48:49], off offset:3584
	v_lshl_add_u64 v[44:45], v[50:51], 0, s[4:5]
	s_mov_b64 s[4:5], 0x3e000
	v_lshl_add_u64 v[76:77], v[50:51], 0, s[4:5]
	s_mov_b32 s4, 0x3d000
	v_add_co_u32_e32 v84, vcc, s4, v50
	s_mov_b32 s4, 0x3f000
	s_nop 0
	v_addc_co_u32_e32 v85, vcc, 0, v51, vcc
	v_add_co_u32_e32 v108, vcc, s4, v50
	global_load_dwordx4 v[52:55], v[84:85], off offset:-4096
	s_nop 0
	v_addc_co_u32_e32 v109, vcc, 0, v51, vcc
	global_load_dwordx4 v[48:51], v[108:109], off offset:-4096
	global_load_dwordx4 v[56:59], v[44:45], off offset:1024
	global_load_dwordx4 v[60:63], v[44:45], off offset:2048
	global_load_dwordx4 v[64:67], v[76:77], off offset:1024
	global_load_dwordx4 v[68:71], v[44:45], off offset:3072
	global_load_dwordx4 v[72:75], v[76:77], off offset:2048
	s_nop 0
	global_load_dwordx4 v[76:79], v[76:77], off offset:3072
	v_pk_mul_f32 v[44:45], v[6:7], v[6:7]
	v_pk_mul_f32 v[80:81], v[4:5], v[4:5]
	v_add_f32_e32 v1, v44, v45
	v_add_f32_e32 v1, v80, v1
	v_pk_mul_f32 v[82:83], v[8:9], v[8:9]
	v_add_f32_e32 v1, v81, v1
	v_add_f32_e32 v1, v82, v1
	v_pk_mul_f32 v[88:89], v[10:11], v[10:11]
	v_add_f32_e32 v1, v83, v1
	v_add_f32_e32 v1, v88, v1
	v_pk_mul_f32 v[90:91], v[12:13], v[12:13]
	v_add_f32_e32 v1, v89, v1
	v_add_f32_e32 v1, v90, v1
	v_pk_mul_f32 v[92:93], v[14:15], v[14:15]
	v_add_f32_e32 v1, v91, v1
	v_add_f32_e32 v1, v92, v1
	v_pk_mul_f32 v[94:95], v[16:17], v[16:17]
	v_add_f32_e32 v1, v93, v1
	v_add_f32_e32 v1, v94, v1
; DEVI unsigned cvt_pk(float lo, float hi) { f32x2 v = {lo, hi}; bf16x2_t b = __builtin_convertvector(v, bf16x2_t); return __builtin_bit_cast(unsigned, b); }
; DEVI float bflo(unsigned w) { return __uint_as_float(w << 16); }
; DEVI float bfhi(unsigned w) { return __uint_as_float(w & 0xffff0000u); }
; DEVI unsigned cvt4_fp8c(float a, float b, float c, float d) { return cvt4_fp8(clamp8(a), clamp8(b), clamp8(c), clamp8(d)); }
; template <int MODE>
; DEVI void phase_rows(const Params& p, int l, char* smem) {
;     ...
;         } else { const bf16_t* src = xres + (size_t)row * DM;
; #pragma unroll
;             for (int i = 0; i < 8; ++i) { const u32x2 t = *(const u32x2*)(src + i * 256 + lane * 4); v[i * 4] = bflo(t[0]); v[i * 4 + 1] = bfhi(t[0]); v[i * 4 + 2] = bflo(t[1]); v[i * 4 + 3] = bfhi(t[1]); }
;     ...
;         float ss = 0.f;
; #pragma unroll
;         for (int i = 0; i < 32; ++i) ss += v[i] * v[i];
;         ss = wave_sum(ss);
;         const float rstd = rsqrtf(ss * (1.f / DM) + EPS);
;         if (MODE == 3) {
; #pragma unroll
;             for (int i = 0; i < 8; ++i) { const f32x4 g = *(const f32x4*)(p.final_norm + i * 256 + lane * 4);
;                 __builtin_nontemporal_store((f32x4){v[i * 4] * rstd * g[0], v[i * 4 + 1] * rstd * g[1], v[i * 4 + 2] * rstd * g[2], v[i * 4 + 3] * rstd * g[3]}, (f32x4*)(p.out + (size_t)row * DM + i * 256 + lane * 4)); }
;             continue;
;         }
; #pragma unroll
;         for (int i = 0; i < 8; ++i) { const f32x4 a = shv[i]; const f32x4 s = scv[i];
; #pragma unroll
;             for (int j = 0; j < 4; ++j) v[i * 4 + j] = v[i * 4 + j] * rstd * (1.f + s[j]) + a[j];
;             if (MODE == 1) *(unsigned*)((unsigned char*)hbuf + (size_t)row * DM + i * 256 + lane * 4) = cvt4_fp8c(v[i * 4], v[i * 4 + 1], v[i * 4 + 2], v[i * 4 + 3]);
;             else *(u32x2*)(hbuf + (size_t)row * DM + i * 256 + lane * 4) = (u32x2){cvt_pk(v[i * 4], v[i * 4 + 1]), cvt_pk(v[i * 4 + 2], v[i * 4 + 3])}; }
	v_pk_mul_f32 v[96:97], v[18:19], v[18:19]
	v_add_f32_e32 v1, v95, v1
	v_add_f32_e32 v1, v96, v1
	v_pk_mul_f32 v[98:99], v[20:21], v[20:21]
	v_add_f32_e32 v1, v97, v1
	v_add_f32_e32 v1, v98, v1
	v_pk_mul_f32 v[100:101], v[22:23], v[22:23]
	v_add_f32_e32 v1, v99, v1
	v_add_f32_e32 v1, v100, v1
	global_load_dwordx4 v[80:83], v[84:85], off
	global_load_dwordx4 v[88:91], v[108:109], off
	v_pk_mul_f32 v[102:103], v[24:25], v[24:25]
	v_add_f32_e32 v1, v101, v1
	v_add_f32_e32 v1, v102, v1
	v_pk_mul_f32 v[104:105], v[26:27], v[26:27]
	v_add_f32_e32 v1, v103, v1
	v_add_f32_e32 v1, v104, v1
	v_pk_mul_f32 v[106:107], v[28:29], v[28:29]
	v_add_f32_e32 v1, v105, v1
	global_load_dwordx4 v[92:95], v[108:109], off offset:1024
	global_load_dwordx4 v[96:99], v[84:85], off offset:1024
	v_add_f32_e32 v1, v106, v1
	v_pk_mul_f32 v[110:111], v[30:31], v[30:31]
	v_add_f32_e32 v1, v107, v1
	v_add_f32_e32 v1, v110, v1
	global_load_dwordx4 v[100:103], v[84:85], off offset:2048
	global_load_dwordx4 v[104:107], v[108:109], off offset:2048
	v_pk_mul_f32 v[112:113], v[32:33], v[32:33]
	v_add_f32_e32 v1, v111, v1
	v_add_f32_e32 v1, v112, v1
	v_pk_mul_f32 v[114:115], v[34:35], v[34:35]
	v_add_f32_e32 v1, v113, v1
	v_add_f32_e32 v1, v114, v1
	v_add_f32_e32 v1, v115, v1
	global_load_dwordx4 v[108:111], v[108:109], off offset:3072
	s_nop 0
	global_load_dwordx4 v[112:115], v[84:85], off offset:3072
	v_lshlrev_b32_e32 v248, 12, v36
	v_mov_b32_e32 v249, 0
	v_lshl_add_u64 v[248:249], v[42:43], 0, v[248:249]
	global_load_dwordx2 v[176:177], v[248:249], off
	global_load_dwordx2 v[178:179], v[248:249], off offset:512
	global_load_dwordx2 v[228:229], v[248:249], off offset:1024
	global_load_dwordx2 v[232:233], v[248:249], off offset:1536
	global_load_dwordx2 v[236:237], v[248:249], off offset:2048
	global_load_dwordx2 v[240:241], v[248:249], off offset:2560
	global_load_dwordx2 v[242:243], v[248:249], off offset:3072
	global_load_dwordx2 v[246:247], v[248:249], off offset:3584
	ds_bpermute_b32 v2, v39, v1
	v_lshl_add_u64 v[44:45], v[46:47], 1, v[40:41]
	s_movk_i32 s4, 0x23ff
	s_waitcnt lgkmcnt(0)
	v_add_f32_e32 v1, v1, v2
	ds_bpermute_b32 v2, v87, v1
	s_waitcnt lgkmcnt(0)
	v_add_f32_e32 v1, v1, v2
	ds_bpermute_b32 v2, v140, v1
	s_waitcnt lgkmcnt(0)
	v_add_f32_e32 v1, v1, v2
	ds_bpermute_b32 v2, v141, v1
	s_waitcnt vmcnt(22)
	v_pk_add_f32 v[46:47], v[48:49], 1.0 op_sel_hi:[1,0]
	s_waitcnt lgkmcnt(0)
	v_add_f32_e32 v1, v1, v2
	ds_bpermute_b32 v2, v142, v1
	s_waitcnt lgkmcnt(0)
	v_add_f32_e32 v1, v1, v2
	ds_bpermute_b32 v2, v143, v1
	s_waitcnt lgkmcnt(0)
	v_add_f32_e32 v1, v1, v2
	v_fmamk_f32 v1, v1, 0x3a000000, v223
	v_mul_f32_e32 v2, 0x4b800000, v1
	v_cmp_gt_f32_e32 vcc, s97, v1
	s_nop 1
	v_cndmask_b32_e32 v1, v1, v2, vcc
	v_rsq_f32_e32 v1, v1
	s_nop 0
	v_mul_f32_e32 v2, 0x45800000, v1
	v_cndmask_b32_e32 v2, v1, v2, vcc
	v_pk_mul_f32 v[6:7], v[6:7], v[2:3] op_sel_hi:[1,0]
	v_pk_mul_f32 v[4:5], v[4:5], v[2:3] op_sel_hi:[1,0]
	v_pk_fma_f32 v[6:7], v[46:47], v[6:7], v[52:53]
	v_pk_add_f32 v[46:47], v[50:51], 1.0 op_sel_hi:[1,0]
	v_cvt_pk_bf16_f32 v6, v6, v7
	v_pk_fma_f32 v[4:5], v[46:47], v[4:5], v[54:55]
	v_cmp_lt_i32_e32 vcc, s4, v36
	v_cvt_pk_bf16_f32 v7, v4, v5
	global_store_dwordx2 v[44:45], v[6:7], off
	v_pk_mul_f32 v[4:5], v[8:9], v[2:3] op_sel_hi:[1,0]
	s_waitcnt vmcnt(20)
	v_pk_add_f32 v[6:7], v[64:65], 1.0 op_sel_hi:[1,0]
	v_pk_add_f32 v[8:9], v[66:67], 1.0 op_sel_hi:[1,0]
	v_pk_fma_f32 v[4:5], v[6:7], v[4:5], v[56:57]
	v_pk_mul_f32 v[6:7], v[10:11], v[2:3] op_sel_hi:[1,0]
	v_cvt_pk_bf16_f32 v4, v4, v5
	v_pk_fma_f32 v[6:7], v[8:9], v[6:7], v[58:59]
	s_waitcnt vmcnt(18)
	v_pk_add_f32 v[8:9], v[74:75], 1.0 op_sel_hi:[1,0]
	v_cvt_pk_bf16_f32 v5, v6, v7
	global_store_dwordx2 v[44:45], v[4:5], off offset:512
	v_pk_mul_f32 v[4:5], v[12:13], v[2:3] op_sel_hi:[1,0]
	v_pk_add_f32 v[6:7], v[72:73], 1.0 op_sel_hi:[1,0]
	s_or_b64 s[42:43], vcc, s[42:43]
	v_pk_fma_f32 v[4:5], v[6:7], v[4:5], v[60:61]
	v_pk_mul_f32 v[6:7], v[14:15], v[2:3] op_sel_hi:[1,0]
	v_cvt_pk_bf16_f32 v4, v4, v5
	v_pk_fma_f32 v[6:7], v[8:9], v[6:7], v[62:63]
	s_waitcnt vmcnt(18)
	v_pk_add_f32 v[8:9], v[78:79], 1.0 op_sel_hi:[1,0]
	v_cvt_pk_bf16_f32 v5, v6, v7
	global_store_dwordx2 v[44:45], v[4:5], off offset:1024
	v_pk_mul_f32 v[4:5], v[16:17], v[2:3] op_sel_hi:[1,0]
	v_pk_add_f32 v[6:7], v[76:77], 1.0 op_sel_hi:[1,0]
	s_nop 0
	v_pk_fma_f32 v[4:5], v[6:7], v[4:5], v[68:69]
	v_pk_mul_f32 v[6:7], v[18:19], v[2:3] op_sel_hi:[1,0]
	v_cvt_pk_bf16_f32 v4, v4, v5
	v_pk_fma_f32 v[6:7], v[8:9], v[6:7], v[70:71]
	s_waitcnt vmcnt(17)
	v_pk_add_f32 v[8:9], v[90:91], 1.0 op_sel_hi:[1,0]
	v_cvt_pk_bf16_f32 v5, v6, v7
	global_store_dwordx2 v[44:45], v[4:5], off offset:1536
	v_pk_mul_f32 v[4:5], v[20:21], v[2:3] op_sel_hi:[1,0]
	v_pk_add_f32 v[6:7], v[88:89], 1.0 op_sel_hi:[1,0]
	s_nop 0
	v_pk_fma_f32 v[4:5], v[6:7], v[4:5], v[80:81]
	v_pk_mul_f32 v[6:7], v[22:23], v[2:3] op_sel_hi:[1,0]
	v_cvt_pk_bf16_f32 v4, v4, v5
	v_pk_fma_f32 v[6:7], v[8:9], v[6:7], v[82:83]
	s_waitcnt vmcnt(17)
	v_pk_add_f32 v[8:9], v[94:95], 1.0 op_sel_hi:[1,0]
	v_cvt_pk_bf16_f32 v5, v6, v7
	global_store_dwordx2 v[44:45], v[4:5], off offset:2048
	v_pk_mul_f32 v[4:5], v[24:25], v[2:3] op_sel_hi:[1,0]
	v_pk_add_f32 v[6:7], v[92:93], 1.0 op_sel_hi:[1,0]
	s_waitcnt vmcnt(17)
	v_pk_fma_f32 v[4:5], v[6:7], v[4:5], v[96:97]
	v_pk_mul_f32 v[6:7], v[26:27], v[2:3] op_sel_hi:[1,0]
	v_cvt_pk_bf16_f32 v4, v4, v5
	v_pk_fma_f32 v[6:7], v[8:9], v[6:7], v[98:99]
	s_waitcnt vmcnt(15)
	v_pk_add_f32 v[8:9], v[106:107], 1.0 op_sel_hi:[1,0]
	v_cvt_pk_bf16_f32 v5, v6, v7
	global_store_dwordx2 v[44:45], v[4:5], off offset:2560
	v_pk_mul_f32 v[4:5], v[28:29], v[2:3] op_sel_hi:[1,0]
	v_pk_add_f32 v[6:7], v[104:105], 1.0 op_sel_hi:[1,0]
	s_nop 0
	v_pk_fma_f32 v[4:5], v[6:7], v[4:5], v[100:101]
	v_pk_mul_f32 v[6:7], v[30:31], v[2:3] op_sel_hi:[1,0]
	v_cvt_pk_bf16_f32 v4, v4, v5
	v_pk_fma_f32 v[6:7], v[8:9], v[6:7], v[102:103]
	s_waitcnt vmcnt(15)
	v_pk_add_f32 v[8:9], v[110:111], 1.0 op_sel_hi:[1,0]
	v_cvt_pk_bf16_f32 v5, v6, v7
	global_store_dwordx2 v[44:45], v[4:5], off offset:3072
	v_pk_mul_f32 v[4:5], v[32:33], v[2:3] op_sel_hi:[1,0]
	v_pk_add_f32 v[6:7], v[108:109], 1.0 op_sel_hi:[1,0]
	s_waitcnt vmcnt(15)
	v_pk_fma_f32 v[4:5], v[6:7], v[4:5], v[112:113]
	v_pk_mul_f32 v[6:7], v[34:35], v[2:3] op_sel_hi:[1,0]
	v_cvt_pk_bf16_f32 v4, v4, v5
	v_pk_fma_f32 v[6:7], v[8:9], v[6:7], v[114:115]
	s_nop 0
	v_cvt_pk_bf16_f32 v5, v6, v7
	global_store_dwordx2 v[44:45], v[4:5], off offset:3584
	s_andn2_b64 exec, exec, s[42:43]
	s_cbranch_execz .LBB0_1908
; DEVI float bflo(unsigned w) { return __uint_as_float(w << 16); }
; DEVI float bfhi(unsigned w) { return __uint_as_float(w & 0xffff0000u); }
; DEVI int obid() { int b = blockIdx.x; asm volatile("" : "+s"(b)); return b; }
; template <int MODE>
; DEVI void phase_rows(const Params& p, int l, char* smem) {
;     ...
;     for (int row = obid() * 8 + wid; row < nrows; row += gridDim.x * 8) {
;         const bool lat = row < NLAT;
;         const int b = lat ? (row >> 11) : ((row - NLAT) >> 8);
;         const int tok = lat ? (row & 2047) : (SEQ + ((row - NLAT) & 255));
;         float v[32];
;         if (MODE == 0) { const float* src = lat ? p.x + (size_t)row * DM : p.ctx + (size_t)(row - NLAT) * DM;
; #pragma unroll
;             for (int i = 0; i < 8; ++i) { const f32x4 t = *(const f32x4*)(src + i * 256 + lane * 4); v[i * 4] = t[0]; v[i * 4 + 1] = t[1]; v[i * 4 + 2] = t[2]; v[i * 4 + 3] = t[3]; }
;         } else { const bf16_t* src = xres + (size_t)row * DM;
; #pragma unroll
;             for (int i = 0; i < 8; ++i) { const u32x2 t = *(const u32x2*)(src + i * 256 + lane * 4); v[i * 4] = bflo(t[0]); v[i * 4 + 1] = bfhi(t[0]); v[i * 4 + 2] = bflo(t[1]); v[i * 4 + 3] = bfhi(t[1]); }
;         }
;         const float* mrow = mod + (size_t)(((MODE == 2) ? l : l) * 5 + (lat ? b : 4)) * 12288;
;         if (MODE == 2 || MODE == 3) {
;             float cacc[32];
; #pragma unroll
;             for (int i = 0; i < 32; ++i) cacc[i] = 0.f;
;             const int* rk = (const int*)(p.ws + WS_RANK) + (size_t)b * 16 * KEYS + tok;
;             const bf16_t* ydn = (const bf16_t*)(p.ws + WS_YDN);
;             const int cap = lat ? 256 : 32;
;             int rke[16];
; #pragma unroll
;             for (int e = 0; e < 16; ++e) rke[e] = rk[e * KEYS];
;             const bf16_t* y0 = ydn; const bf16_t* y1 = ydn; const bf16_t* y2 = ydn; const bf16_t* y3 = ydn; int ny = 0;
; #pragma unroll
;             for (int e = 0; e < 16; ++e) {
;                 const int r = rke[e];
;                 if (r < cap) {
;                     const int slot = lat ? (b * 256 + r) : (1024 + b * 32 + r);
;                     const bf16_t* yr = ydn + ((size_t)e * MSLOT + slot) * DM;
;                     if (ny == 0) y0 = yr; else if (ny == 1) y1 = yr; else if (ny == 2) y2 = yr; else if (ny == 3) y3 = yr;
.LBB0_1684:
	v_cmp_gt_i32_e32 vcc, s90, v36
	v_cmp_lt_i32_e64 s[38:39], s73, v36
	s_and_saveexec_b64 s[4:5], s[38:39]
	s_xor_b64 s[16:17], exec, s[4:5]
	v_add_u32_e32 v1, 0xffffe000, v36
	v_lshrrev_b32_e32 v2, 8, v1
	v_mov_b32_e32 v6, v2
	v_mov_b64_e32 v[4:5], v[2:3]
	s_or_saveexec_b64 s[16:17], s[16:17]
	v_mov_b64_e32 v[50:51], 0xc000
	v_mov_b32_e32 v78, 32
	s_xor_b64 exec, exec, s[16:17]
	v_ashrrev_i32_e32 v4, 11, v36
	v_ashrrev_i32_e32 v5, 31, v4
	v_mul_hi_i32_i24_e32 v51, 0x3000, v4
	v_mul_i32_i24_e32 v50, 0x3000, v4
	v_mov_b32_e32 v78, 0x100
	v_mov_b32_e32 v6, v4
	s_or_b64 exec, exec, s[16:17]
	s_movk_i32 s4, 0x800
	v_or_b32_sdwa v1, v36, s4 dst_sel:DWORD dst_unused:UNUSED_PAD src0_sel:BYTE_0 src1_sel:DWORD
	v_ashrrev_i32_e32 v37, 31, v36
	v_readlane_b32 s4, v254, 22
	v_lshlrev_b64 v[8:9], 12, v[36:37]
	v_readlane_b32 s5, v254, 23
	v_lshl_add_u64 v[44:45], v[42:43], 0, v[8:9]
	s_mov_b32 s6, 0x24000
	v_mov_b64_e32 v[8:9], s[4:5]
	v_and_b32_e32 v2, 0x7ff, v36
	v_mad_u64_u32 v[8:9], s[4:5], v4, s6, v[8:9]
	v_cndmask_b32_e32 v1, v1, v2, vcc
	v_mov_b32_e32 v2, v9
	v_mad_u64_u32 v[4:5], s[4:5], v5, s6, v[2:3]
	v_mov_b32_e32 v9, v4
	v_lshlrev_b32_e32 v2, 2, v1
	v_lshl_add_u64 v[8:9], v[8:9], 0, v[2:3]
	v_add_co_u32_e64 v4, s[38:39], s90, v8
	s_movk_i32 s4, 0x4000
	s_nop 0
	v_addc_co_u32_e64 v5, s[38:39], 0, v9, s[38:39]
	v_add_co_u32_e64 v10, s[38:39], s4, v8
	s_movk_i32 s4, 0x6000
	s_nop 0
	v_addc_co_u32_e64 v11, s[38:39], 0, v9, s[38:39]
	s_waitcnt vmcnt(8)
	v_mov_b64_e32 v[64:65], v[176:177]
	v_mov_b64_e32 v[62:63], v[178:179]
	v_mov_b64_e32 v[60:61], v[228:229]
	v_mov_b64_e32 v[58:59], v[232:233]
	v_mov_b64_e32 v[56:57], v[236:237]
	v_mov_b64_e32 v[54:55], v[240:241]
	v_mov_b64_e32 v[52:53], v[242:243]
	v_mov_b64_e32 v[48:49], v[246:247]
	ds_bpermute_b32 v7, v203, v198
	v_mov_b64_e32 v[66:67], s[70:71]
	ds_bpermute_b32 v5, v204, v198
	s_nop 0
	ds_bpermute_b32 v4, v205, v198
	v_add_co_u32_e64 v10, s[38:39], s4, v8
	s_mov_b32 s4, 0x9000
	s_nop 0
	v_addc_co_u32_e64 v11, s[38:39], 0, v9, s[38:39]
	ds_bpermute_b32 v2, v206, v198
	v_add_co_u32_e64 v10, s[38:39], s4, v8
	s_mov_b32 s4, 0xb000
	s_nop 0
	v_addc_co_u32_e64 v11, s[38:39], 0, v9, s[38:39]
	ds_bpermute_b32 v74, v207, v198
	v_add_co_u32_e64 v10, s[38:39], s4, v8
	s_mov_b32 s4, 0xd000
	s_nop 0
	v_addc_co_u32_e64 v11, s[38:39], 0, v9, s[38:39]
	ds_bpermute_b32 v91, v208, v198
	v_add_co_u32_e64 v10, s[38:39], s4, v8
	s_mov_b32 s4, 0x12000
	s_nop 0
	v_addc_co_u32_e64 v11, s[38:39], 0, v9, s[38:39]
	ds_bpermute_b32 v90, v209, v198
	v_add_co_u32_e64 v10, s[38:39], s62, v8
	s_nop 1
	v_addc_co_u32_e64 v11, s[38:39], 0, v9, s[38:39]
	ds_bpermute_b32 v89, v210, v198
	v_add_co_u32_e64 v10, s[38:39], s4, v8
	s_mov_b32 s4, 0x14000
	s_nop 0
	v_addc_co_u32_e64 v11, s[38:39], 0, v9, s[38:39]
	ds_bpermute_b32 v1, v211, v198
	v_add_co_u32_e64 v10, s[38:39], s4, v8
	s_mov_b32 s4, 0x16000
	s_nop 0
	v_addc_co_u32_e64 v11, s[38:39], 0, v9, s[38:39]
	ds_bpermute_b32 v86, v212, v198
	v_add_co_u32_e64 v10, s[38:39], s4, v8
	s_mov_b32 s4, 0x18000
	s_nop 0
	v_addc_co_u32_e64 v11, s[38:39], 0, v9, s[38:39]
	ds_bpermute_b32 v85, v213, v198
	v_add_co_u32_e64 v10, s[38:39], s4, v8
	s_mov_b32 s4, 0x1b000
	s_nop 0
	v_addc_co_u32_e64 v11, s[38:39], 0, v9, s[38:39]
	ds_bpermute_b32 v84, v214, v198
	v_add_co_u32_e64 v10, s[38:39], s4, v8
	s_mov_b32 s4, 0x1d000
	s_nop 0
	v_addc_co_u32_e64 v11, s[38:39], 0, v9, s[38:39]
	ds_bpermute_b32 v83, v215, v198
	v_add_co_u32_e64 v10, s[38:39], s4, v8
	s_mov_b32 s4, 0x1f000
	s_nop 0
	v_addc_co_u32_e64 v11, s[38:39], 0, v9, s[38:39]
	ds_bpermute_b32 v82, v216, v198
	v_add_co_u32_e64 v10, s[38:39], s4, v8
	s_mov_b32 s4, 0x21000
	s_nop 0
	v_addc_co_u32_e64 v11, s[38:39], 0, v9, s[38:39]
	v_add_co_u32_e64 v8, s[38:39], s4, v8
	ds_bpermute_b32 v81, v217, v198
	s_nop 0
	v_addc_co_u32_e64 v9, s[38:39], 0, v9, s[38:39]
	ds_bpermute_b32 v79, v218, v198
	v_mov_b32_e32 v9, 0x400
	v_lshlrev_b32_e32 v8, 8, v6
	v_lshl_add_u32 v6, v6, 5, v9
	v_cndmask_b32_e32 v80, v6, v8, vcc
	s_waitcnt lgkmcnt(0)
	v_mov_b32_e32 v198, v199
	v_mov_b32_e32 v199, v200
	v_mov_b32_e32 v200, v201
	v_mov_b32_e32 v201, v202
	v_add_u32_e32 v6, v7, v80
	v_cmp_lt_i32_e32 vcc, v7, v78
	v_ashrrev_i32_e32 v7, 31, v6
	v_lshlrev_b64 v[6:7], 12, v[6:7]
	v_cndmask_b32_e32 v7, 0, v7, vcc
	v_cndmask_b32_e32 v6, 0, v6, vcc
	v_cndmask_b32_e64 v88, 0, 1, vcc
	v_lshl_add_u64 v[72:73], s[70:71], 0, v[6:7]
	v_cmp_lt_i32_e64 s[38:39], v5, v78
	s_and_saveexec_b64 s[16:17], s[38:39]
	s_cbranch_execz .LBB0_1690
	v_add_u32_e32 v6, v5, v80
	v_ashrrev_i32_e32 v7, 31, v6
	v_lshlrev_b64 v[6:7], 12, v[6:7]
	v_lshl_add_u64 v[6:7], s[70:71], 0, v[6:7]
	s_mov_b64 s[4:5], 0x500000
	v_lshl_add_u64 v[6:7], v[6:7], 0, s[4:5]
	v_mov_b32_e32 v5, s71
	v_cndmask_b32_e32 v67, v5, v7, vcc
	v_mov_b32_e32 v5, s70
	v_cndmask_b32_e32 v66, v5, v6, vcc
	v_cndmask_b32_e32 v73, v7, v73, vcc
	v_cndmask_b32_e32 v72, v6, v72, vcc
	v_cndmask_b32_e64 v88, 1, 2, vcc
.LBB0_1690:
	s_or_b64 exec, exec, s[16:17]
	v_cmp_lt_i32_e32 vcc, v4, v78
	v_mov_b64_e32 v[68:69], s[70:71]
	s_and_saveexec_b64 s[16:17], vcc
	s_cbranch_execz .LBB0_1696
	v_cmp_lt_i32_e32 vcc, 1, v88
	s_and_saveexec_b64 s[4:5], vcc
	s_xor_b64 s[28:29], exec, s[4:5]
	s_or_saveexec_b64 s[28:29], s[28:29]
	v_add_u32_e32 v4, v4, v80
	v_ashrrev_i32_e32 v5, 31, v4
	v_lshlrev_b64 v[4:5], 12, v[4:5]
	v_lshl_add_u64 v[4:5], s[70:71], 0, v[4:5]
	s_mov_b64 s[4:5], 0xa00000
	v_lshl_add_u64 v[68:69], v[4:5], 0, s[4:5]
	s_xor_b64 exec, exec, s[28:29]
	s_cbranch_execz .LBB0_1695
	v_cmp_eq_u32_e32 vcc, 1, v88
	v_mov_b64_e32 v[4:5], v[68:69]
	s_and_saveexec_b64 s[34:35], vcc
	v_mov_b64_e32 v[4:5], v[72:73]
	v_mov_b64_e32 v[66:67], v[68:69]
	s_or_b64 exec, exec, s[34:35]
	v_mov_b64_e32 v[68:69], s[70:71]
	v_mov_b64_e32 v[72:73], v[4:5]

; DEVI float bflo(unsigned w) { return __uint_as_float(w << 16); }
; DEVI float bfhi(unsigned w) { return __uint_as_float(w & 0xffff0000u); }
; template <int MODE>
; DEVI void phase_rows(const Params& p, int l, char* smem) {
;     ...
;             for (int e = 0; e < 16; ++e) {
;                 const int r = rke[e];
;                 if (r < cap) {
;                     const int slot = lat ? (b * 256 + r) : (1024 + b * 32 + r);
;                     const bf16_t* yr = ydn + ((size_t)e * MSLOT + slot) * DM;
;                     if (ny == 0) y0 = yr; else if (ny == 1) y1 = yr; else if (ny == 2) y2 = yr; else if (ny == 3) y3 = yr;
;                     else {
; #pragma unroll
;                         for (int i = 0; i < 8; ++i) { const u32x2 w = *(const u32x2*)(yr + i * 256 + lane * 4);
;                             cacc[i * 4] += bflo(w[0]); cacc[i * 4 + 1] += bfhi(w[0]); cacc[i * 4 + 2] += bflo(w[1]); cacc[i * 4 + 3] += bfhi(w[1]); }
;                     }
;                     ++ny;
.LBB0_1696:
	s_or_b64 exec, exec, s[16:17]
	v_lshlrev_b64 v[46:47], 11, v[36:37]
	v_cmp_lt_i32_e32 vcc, v2, v78
	v_mov_b64_e32 v[70:71], s[70:71]
	s_and_saveexec_b64 s[16:17], vcc
	s_cbranch_execz .LBB0_1706
	v_add_u32_e32 v4, v2, v80
	v_ashrrev_i32_e32 v5, 31, v4
	v_lshlrev_b64 v[4:5], 12, v[4:5]
	v_lshl_add_u64 v[4:5], s[70:71], 0, v[4:5]
	s_mov_b64 s[4:5], 0xf00000
	v_lshl_add_u64 v[70:71], v[4:5], 0, s[4:5]
	v_cmp_lt_i32_e32 vcc, 1, v88
	s_and_saveexec_b64 s[4:5], vcc
	s_xor_b64 s[28:29], exec, s[4:5]
	s_cbranch_execz .LBB0_1701
	v_cmp_lt_i32_e32 vcc, 2, v88
	s_and_saveexec_b64 s[4:5], vcc
	s_xor_b64 s[34:35], exec, s[4:5]
	s_andn2_saveexec_b64 s[34:35], s[34:35]
	v_mov_b64_e32 v[68:69], v[70:71]
	v_mov_b64_e32 v[70:71], s[70:71]
	s_or_b64 exec, exec, s[34:35]

; DEVI float bflo(unsigned w) { return __uint_as_float(w << 16); }
; DEVI float bfhi(unsigned w) { return __uint_as_float(w & 0xffff0000u); }
; template <int MODE>
; DEVI void phase_rows(const Params& p, int l, char* smem) {
;     ...
;             float cacc[32];
; #pragma unroll
;             for (int i = 0; i < 32; ++i) cacc[i] = 0.f;
;             const int* rk = (const int*)(p.ws + WS_RANK) + (size_t)b * 16 * KEYS + tok;
;             const bf16_t* ydn = (const bf16_t*)(p.ws + WS_YDN);
;             const int cap = lat ? 256 : 32;
;             int rke[16];
; #pragma unroll
;             for (int e = 0; e < 16; ++e) rke[e] = rk[e * KEYS];
;             const bf16_t* y0 = ydn; const bf16_t* y1 = ydn; const bf16_t* y2 = ydn; const bf16_t* y3 = ydn; int ny = 0;
; #pragma unroll
;             for (int e = 0; e < 16; ++e) {
;                 const int r = rke[e];
;                 if (r < cap) {
;                     const int slot = lat ? (b * 256 + r) : (1024 + b * 32 + r);
;                     const bf16_t* yr = ydn + ((size_t)e * MSLOT + slot) * DM;
;                     if (ny == 0) y0 = yr; else if (ny == 1) y1 = yr; else if (ny == 2) y2 = yr; else if (ny == 3) y3 = yr;
;                     else {
; #pragma unroll
;                         for (int i = 0; i < 8; ++i) { const u32x2 w = *(const u32x2*)(yr + i * 256 + lane * 4);
;                             cacc[i * 4] += bflo(w[0]); cacc[i * 4 + 1] += bfhi(w[0]); cacc[i * 4 + 2] += bflo(w[1]); cacc[i * 4 + 3] += bfhi(w[1]); }
;                     }
;                     ++ny;
.LBB0_1706:
	s_or_b64 exec, exec, s[16:17]
	v_mov_b32_e32 v4, v3
	v_mov_b32_e32 v5, v3
	v_mov_b32_e32 v6, v3
	v_mov_b32_e32 v7, v3
	v_mov_b32_e32 v8, v3
	v_mov_b32_e32 v9, v3
	v_mov_b32_e32 v10, v3
	v_mov_b32_e32 v11, v3
	v_mov_b32_e32 v12, v3
	v_mov_b32_e32 v13, v3
	v_mov_b32_e32 v14, v3
	v_mov_b32_e32 v15, v3
	v_mov_b32_e32 v16, v3
	v_mov_b32_e32 v17, v3
	v_mov_b32_e32 v18, v3
	v_mov_b32_e32 v19, v3
	v_mov_b32_e32 v20, v3
	v_mov_b32_e32 v21, v3
	v_mov_b32_e32 v22, v3
	v_mov_b32_e32 v23, v3
	v_mov_b32_e32 v24, v3
	v_mov_b32_e32 v25, v3
	v_mov_b32_e32 v26, v3
	v_mov_b32_e32 v27, v3
	v_mov_b32_e32 v28, v3
	v_mov_b32_e32 v29, v3
	v_mov_b32_e32 v30, v3
	v_mov_b32_e32 v31, v3
	v_mov_b32_e32 v32, v3
	v_mov_b32_e32 v33, v3
	v_mov_b32_e32 v2, v3
	v_mov_b64_e32 v[34:35], v[32:33]
	v_cmp_lt_i32_e32 vcc, v74, v78
	v_mov_b64_e32 v[32:33], v[30:31]
	v_mov_b64_e32 v[30:31], v[28:29]
	v_mov_b64_e32 v[28:29], v[26:27]
	v_mov_b64_e32 v[26:27], v[24:25]
	v_mov_b64_e32 v[24:25], v[22:23]
	v_mov_b64_e32 v[22:23], v[20:21]
	v_mov_b64_e32 v[20:21], v[18:19]
	v_mov_b64_e32 v[18:19], v[16:17]
	v_mov_b64_e32 v[16:17], v[14:15]
	v_mov_b64_e32 v[14:15], v[12:13]
	v_mov_b64_e32 v[12:13], v[10:11]
	v_mov_b64_e32 v[10:11], v[8:9]
	v_mov_b64_e32 v[8:9], v[6:7]
	v_mov_b64_e32 v[6:7], v[4:5]
	v_mov_b64_e32 v[4:5], v[2:3]
	s_and_saveexec_b64 s[16:17], vcc
	s_cbranch_execz .LBB0_1802
	v_add_u32_e32 v4, v74, v80
	v_ashrrev_i32_e32 v5, 31, v4
	v_lshlrev_b64 v[4:5], 12, v[4:5]
	v_lshl_add_u64 v[4:5], s[70:71], 0, v[4:5]
	s_mov_b64 s[4:5], 0x1400000
	v_lshl_add_u64 v[74:75], v[4:5], 0, s[4:5]
	v_cmp_lt_i32_e32 vcc, 1, v88
	s_and_saveexec_b64 s[4:5], vcc
	s_xor_b64 s[38:39], exec, s[4:5]
	s_cbranch_execz .LBB0_1717
	v_cmp_lt_i32_e32 vcc, 2, v88
	s_and_saveexec_b64 s[4:5], vcc
	s_xor_b64 s[28:29], exec, s[4:5]
	s_cbranch_execz .LBB0_1714
	v_cmp_ne_u32_e32 vcc, 3, v88
	s_and_saveexec_b64 s[4:5], vcc
	s_xor_b64 s[34:35], exec, s[4:5]
	s_cbranch_execz .LBB0_1711
	v_lshlrev_b32_e32 v2, 1, v38
	v_lshl_add_u64 v[32:33], v[74:75], 0, v[2:3]
	global_load_dwordx2 v[6:7], v[32:33], off
	global_load_dwordx2 v[10:11], v[32:33], off offset:512
	global_load_dwordx2 v[14:15], v[32:33], off offset:1024
	global_load_dwordx2 v[18:19], v[32:33], off offset:1536
	global_load_dwordx2 v[22:23], v[32:33], off offset:2048
	global_load_dwordx2 v[26:27], v[32:33], off offset:2560
	global_load_dwordx2 v[30:31], v[32:33], off offset:3072
	global_load_dwordx2 v[34:35], v[32:33], off offset:3584
	s_waitcnt vmcnt(7)
	v_lshlrev_b32_e32 v4, 16, v6
	v_and_b32_e32 v5, 0xffff0000, v6
	v_lshlrev_b32_e32 v6, 16, v7
	v_and_b32_e32 v7, 0xffff0000, v7
	s_waitcnt vmcnt(6)
	v_lshlrev_b32_e32 v8, 16, v10
	v_and_b32_e32 v9, 0xffff0000, v10
	v_lshlrev_b32_e32 v10, 16, v11
	v_and_b32_e32 v11, 0xffff0000, v11
	s_waitcnt vmcnt(5)
	v_lshlrev_b32_e32 v12, 16, v14
	v_and_b32_e32 v13, 0xffff0000, v14
	v_lshlrev_b32_e32 v14, 16, v15
	v_and_b32_e32 v15, 0xffff0000, v15
	s_waitcnt vmcnt(4)
	v_lshlrev_b32_e32 v16, 16, v18
	v_and_b32_e32 v17, 0xffff0000, v18
	v_lshlrev_b32_e32 v18, 16, v19
	v_and_b32_e32 v19, 0xffff0000, v19
	s_waitcnt vmcnt(3)
	v_lshlrev_b32_e32 v20, 16, v22
	v_and_b32_e32 v21, 0xffff0000, v22
	v_lshlrev_b32_e32 v22, 16, v23
	v_and_b32_e32 v23, 0xffff0000, v23
	s_waitcnt vmcnt(2)
	v_lshlrev_b32_e32 v24, 16, v26
	v_and_b32_e32 v25, 0xffff0000, v26
	v_lshlrev_b32_e32 v26, 16, v27
	v_and_b32_e32 v27, 0xffff0000, v27
	s_waitcnt vmcnt(1)
	v_lshlrev_b32_e32 v28, 16, v30
	v_and_b32_e32 v29, 0xffff0000, v30
	v_lshlrev_b32_e32 v30, 16, v31
	v_and_b32_e32 v31, 0xffff0000, v31
	s_waitcnt vmcnt(0)
	v_lshlrev_b32_e32 v32, 16, v34
	v_and_b32_e32 v33, 0xffff0000, v34
	v_lshlrev_b32_e32 v34, 16, v35
	v_and_b32_e32 v35, 0xffff0000, v35
	v_pk_add_f32 v[4:5], v[4:5], 0 op_sel_hi:[1,0]
	v_pk_add_f32 v[6:7], v[6:7], 0 op_sel_hi:[1,0]
	v_pk_add_f32 v[8:9], v[8:9], 0 op_sel_hi:[1,0]
	v_pk_add_f32 v[10:11], v[10:11], 0 op_sel_hi:[1,0]
	v_pk_add_f32 v[12:13], v[12:13], 0 op_sel_hi:[1,0]
	v_pk_add_f32 v[14:15], v[14:15], 0 op_sel_hi:[1,0]
	v_pk_add_f32 v[16:17], v[16:17], 0 op_sel_hi:[1,0]
	v_pk_add_f32 v[18:19], v[18:19], 0 op_sel_hi:[1,0]
	v_pk_add_f32 v[20:21], v[20:21], 0 op_sel_hi:[1,0]
	v_pk_add_f32 v[22:23], v[22:23], 0 op_sel_hi:[1,0]
	v_pk_add_f32 v[24:25], v[24:25], 0 op_sel_hi:[1,0]
	v_pk_add_f32 v[26:27], v[26:27], 0 op_sel_hi:[1,0]
	v_pk_add_f32 v[28:29], v[28:29], 0 op_sel_hi:[1,0]
	v_pk_add_f32 v[30:31], v[30:31], 0 op_sel_hi:[1,0]
	v_pk_add_f32 v[32:33], v[32:33], 0 op_sel_hi:[1,0]
	v_pk_add_f32 v[34:35], v[34:35], 0 op_sel_hi:[1,0]

; DEVI float bflo(unsigned w) { return __uint_as_float(w << 16); }
; DEVI float bfhi(unsigned w) { return __uint_as_float(w & 0xffff0000u); }
; template <int MODE>
; DEVI void phase_rows(const Params& p, int l, char* smem) {
;     ...
;             for (int e = 0; e < 16; ++e) {
;                 const int r = rke[e];
;                 if (r < cap) {
;                     const int slot = lat ? (b * 256 + r) : (1024 + b * 32 + r);
;                     const bf16_t* yr = ydn + ((size_t)e * MSLOT + slot) * DM;
;                     if (ny == 0) y0 = yr; else if (ny == 1) y1 = yr; else if (ny == 2) y2 = yr; else if (ny == 3) y3 = yr;
;                     else {
; #pragma unroll
;                         for (int i = 0; i < 8; ++i) { const u32x2 w = *(const u32x2*)(yr + i * 256 + lane * 4);
;                             cacc[i * 4] += bflo(w[0]); cacc[i * 4 + 1] += bfhi(w[0]); cacc[i * 4 + 2] += bflo(w[1]); cacc[i * 4 + 3] += bfhi(w[1]); }
;                     }
;                     ++ny;
;                 }
;             }
.LBB0_1721:
	s_or_b64 exec, exec, s[28:29]
	v_add_u32_e32 v88, 1, v88
	s_or_b64 exec, exec, s[16:17]
	v_cmp_lt_i32_e32 vcc, v91, v78
	s_and_saveexec_b64 s[16:17], vcc
	s_cbranch_execnz .LBB0_1803
.LBB0_1722:
	s_or_b64 exec, exec, s[16:17]
	v_cmp_lt_i32_e32 vcc, v90, v78
	s_and_saveexec_b64 s[16:17], vcc
	s_cbranch_execz .LBB0_1818

; DEVI float bflo(unsigned w) { return __uint_as_float(w << 16); }
; DEVI float bfhi(unsigned w) { return __uint_as_float(w & 0xffff0000u); }
; template <int MODE>
; DEVI void phase_rows(const Params& p, int l, char* smem) {
;     ...
;             for (int e = 0; e < 16; ++e) {
;                 const int r = rke[e];
;                 if (r < cap) {
;                     const int slot = lat ? (b * 256 + r) : (1024 + b * 32 + r);
;                     const bf16_t* yr = ydn + ((size_t)e * MSLOT + slot) * DM;
;                     if (ny == 0) y0 = yr; else if (ny == 1) y1 = yr; else if (ny == 2) y2 = yr; else if (ny == 3) y3 = yr;
;                     else {
; #pragma unroll
;                         for (int i = 0; i < 8; ++i) { const u32x2 w = *(const u32x2*)(yr + i * 256 + lane * 4);
;                             cacc[i * 4] += bflo(w[0]); cacc[i * 4 + 1] += bfhi(w[0]); cacc[i * 4 + 2] += bflo(w[1]); cacc[i * 4 + 3] += bfhi(w[1]); }
;                     }
;                     ++ny;
;                 }
;             }
.LBB0_1737:
	s_or_b64 exec, exec, s[28:29]
	v_add_u32_e32 v88, 1, v88
	s_or_b64 exec, exec, s[16:17]
	v_cmp_lt_i32_e32 vcc, v89, v78
	s_and_saveexec_b64 s[16:17], vcc
	s_cbranch_execnz .LBB0_1819
.LBB0_1738:
	s_or_b64 exec, exec, s[16:17]
	v_cmp_lt_i32_e32 vcc, v1, v78
	s_and_saveexec_b64 s[16:17], vcc
	s_cbranch_execz .LBB0_1834

; DEVI float bflo(unsigned w) { return __uint_as_float(w << 16); }
; DEVI float bfhi(unsigned w) { return __uint_as_float(w & 0xffff0000u); }
; template <int MODE>
; DEVI void phase_rows(const Params& p, int l, char* smem) {
;     ...
;             for (int e = 0; e < 16; ++e) {
;                 const int r = rke[e];
;                 if (r < cap) {
;                     const int slot = lat ? (b * 256 + r) : (1024 + b * 32 + r);
;                     const bf16_t* yr = ydn + ((size_t)e * MSLOT + slot) * DM;
;                     if (ny == 0) y0 = yr; else if (ny == 1) y1 = yr; else if (ny == 2) y2 = yr; else if (ny == 3) y3 = yr;
;                     else {
; #pragma unroll
;                         for (int i = 0; i < 8; ++i) { const u32x2 w = *(const u32x2*)(yr + i * 256 + lane * 4);
;                             cacc[i * 4] += bflo(w[0]); cacc[i * 4 + 1] += bfhi(w[0]); cacc[i * 4 + 2] += bflo(w[1]); cacc[i * 4 + 3] += bfhi(w[1]); }
;                     }
;                     ++ny;
;                 }
;             }
.LBB0_1753:
	s_or_b64 exec, exec, s[28:29]
	v_add_u32_e32 v88, 1, v88
	s_or_b64 exec, exec, s[16:17]
	v_cmp_lt_i32_e32 vcc, v86, v78
	s_and_saveexec_b64 s[16:17], vcc
	s_cbranch_execnz .LBB0_1835
.LBB0_1754:
	s_or_b64 exec, exec, s[16:17]
	v_cmp_lt_i32_e32 vcc, v85, v78
	s_and_saveexec_b64 s[16:17], vcc
	s_cbranch_execz .LBB0_1850

; DEVI float bflo(unsigned w) { return __uint_as_float(w << 16); }
; DEVI float bfhi(unsigned w) { return __uint_as_float(w & 0xffff0000u); }
; template <int MODE>
; DEVI void phase_rows(const Params& p, int l, char* smem) {
;     ...
;             for (int e = 0; e < 16; ++e) {
;                 const int r = rke[e];
;                 if (r < cap) {
;                     const int slot = lat ? (b * 256 + r) : (1024 + b * 32 + r);
;                     const bf16_t* yr = ydn + ((size_t)e * MSLOT + slot) * DM;
;                     if (ny == 0) y0 = yr; else if (ny == 1) y1 = yr; else if (ny == 2) y2 = yr; else if (ny == 3) y3 = yr;
;                     else {
; #pragma unroll
;                         for (int i = 0; i < 8; ++i) { const u32x2 w = *(const u32x2*)(yr + i * 256 + lane * 4);
;                             cacc[i * 4] += bflo(w[0]); cacc[i * 4 + 1] += bfhi(w[0]); cacc[i * 4 + 2] += bflo(w[1]); cacc[i * 4 + 3] += bfhi(w[1]); }
;                     }
;                     ++ny;
;                 }
;             }
.LBB0_1769:
	s_or_b64 exec, exec, s[28:29]
	v_add_u32_e32 v88, 1, v88
	s_or_b64 exec, exec, s[16:17]
	v_cmp_lt_i32_e32 vcc, v84, v78
	s_and_saveexec_b64 s[16:17], vcc
	s_cbranch_execnz .LBB0_1851
.LBB0_1770:
	s_or_b64 exec, exec, s[16:17]
	v_cmp_lt_i32_e32 vcc, v83, v78
	s_and_saveexec_b64 s[16:17], vcc
	s_cbranch_execz .LBB0_1866

; DEVI float bflo(unsigned w) { return __uint_as_float(w << 16); }
; DEVI float bfhi(unsigned w) { return __uint_as_float(w & 0xffff0000u); }
; template <int MODE>
; DEVI void phase_rows(const Params& p, int l, char* smem) {
;     ...
;             for (int e = 0; e < 16; ++e) {
;                 const int r = rke[e];
;                 if (r < cap) {
;                     const int slot = lat ? (b * 256 + r) : (1024 + b * 32 + r);
;                     const bf16_t* yr = ydn + ((size_t)e * MSLOT + slot) * DM;
;                     if (ny == 0) y0 = yr; else if (ny == 1) y1 = yr; else if (ny == 2) y2 = yr; else if (ny == 3) y3 = yr;
;                     else {
; #pragma unroll
;                         for (int i = 0; i < 8; ++i) { const u32x2 w = *(const u32x2*)(yr + i * 256 + lane * 4);
;                             cacc[i * 4] += bflo(w[0]); cacc[i * 4 + 1] += bfhi(w[0]); cacc[i * 4 + 2] += bflo(w[1]); cacc[i * 4 + 3] += bfhi(w[1]); }
;                     }
;                     ++ny;
;                 }
;             }
.LBB0_1785:
	s_or_b64 exec, exec, s[28:29]
	v_add_u32_e32 v88, 1, v88
	s_or_b64 exec, exec, s[16:17]
	v_cmp_lt_i32_e32 vcc, v82, v78
	s_and_saveexec_b64 s[16:17], vcc
	s_cbranch_execnz .LBB0_1867
.LBB0_1786:
	s_or_b64 exec, exec, s[16:17]
	v_cmp_lt_i32_e32 vcc, v81, v78
	s_and_saveexec_b64 s[16:17], vcc
	s_cbranch_execz .LBB0_1882

; DEVI float bflo(unsigned w) { return __uint_as_float(w << 16); }
; DEVI float bfhi(unsigned w) { return __uint_as_float(w & 0xffff0000u); }
; template <int MODE>
; DEVI void phase_rows(const Params& p, int l, char* smem) {
;     ...
;             for (int e = 0; e < 16; ++e) {
;                 const int r = rke[e];
;                 if (r < cap) {
;                     const int slot = lat ? (b * 256 + r) : (1024 + b * 32 + r);
;                     const bf16_t* yr = ydn + ((size_t)e * MSLOT + slot) * DM;
;                     if (ny == 0) y0 = yr; else if (ny == 1) y1 = yr; else if (ny == 2) y2 = yr; else if (ny == 3) y3 = yr;
;                     else {
; #pragma unroll
;                         for (int i = 0; i < 8; ++i) { const u32x2 w = *(const u32x2*)(yr + i * 256 + lane * 4);
;                             cacc[i * 4] += bflo(w[0]); cacc[i * 4 + 1] += bfhi(w[0]); cacc[i * 4 + 2] += bflo(w[1]); cacc[i * 4 + 3] += bfhi(w[1]); }
;                     }
;                     ++ny;
;                 }
;             }
.LBB0_1801:
	s_or_b64 exec, exec, s[28:29]
	v_add_u32_e32 v88, 1, v88
	s_or_b64 exec, exec, s[16:17]
	v_cmp_lt_i32_e32 vcc, v79, v78
	s_and_saveexec_b64 s[16:17], vcc
	s_cbranch_execz .LBB0_1683
	s_branch .LBB0_1883
.LBB0_1802:
	s_or_b64 exec, exec, s[16:17]
	v_cmp_lt_i32_e32 vcc, v91, v78
	s_and_saveexec_b64 s[16:17], vcc
	s_cbranch_execz .LBB0_1722

; DEVI float bflo(unsigned w) { return __uint_as_float(w << 16); }
; DEVI float bfhi(unsigned w) { return __uint_as_float(w & 0xffff0000u); }
; template <int MODE>
; DEVI void phase_rows(const Params& p, int l, char* smem) {
;     ...
;             for (int e = 0; e < 16; ++e) {
;                 const int r = rke[e];
;                 if (r < cap) {
;                     const int slot = lat ? (b * 256 + r) : (1024 + b * 32 + r);
;                     const bf16_t* yr = ydn + ((size_t)e * MSLOT + slot) * DM;
;                     if (ny == 0) y0 = yr; else if (ny == 1) y1 = yr; else if (ny == 2) y2 = yr; else if (ny == 3) y3 = yr;
;                     else {
; #pragma unroll
;                         for (int i = 0; i < 8; ++i) { const u32x2 w = *(const u32x2*)(yr + i * 256 + lane * 4);
;                             cacc[i * 4] += bflo(w[0]); cacc[i * 4 + 1] += bfhi(w[0]); cacc[i * 4 + 2] += bflo(w[1]); cacc[i * 4 + 3] += bfhi(w[1]); }
;                     }
;                     ++ny;
;                 }
;             }
.LBB0_1817:
	s_or_b64 exec, exec, s[28:29]
	v_add_u32_e32 v88, 1, v88
	s_or_b64 exec, exec, s[16:17]
	v_cmp_lt_i32_e32 vcc, v90, v78
	s_and_saveexec_b64 s[16:17], vcc
	s_cbranch_execnz .LBB0_1723
.LBB0_1818:
	s_or_b64 exec, exec, s[16:17]
	v_cmp_lt_i32_e32 vcc, v89, v78
	s_and_saveexec_b64 s[16:17], vcc
	s_cbranch_execz .LBB0_1738

; DEVI float bflo(unsigned w) { return __uint_as_float(w << 16); }
; DEVI float bfhi(unsigned w) { return __uint_as_float(w & 0xffff0000u); }
; template <int MODE>
; DEVI void phase_rows(const Params& p, int l, char* smem) {
;     ...
;             for (int e = 0; e < 16; ++e) {
;                 const int r = rke[e];
;                 if (r < cap) {
;                     const int slot = lat ? (b * 256 + r) : (1024 + b * 32 + r);
;                     const bf16_t* yr = ydn + ((size_t)e * MSLOT + slot) * DM;
;                     if (ny == 0) y0 = yr; else if (ny == 1) y1 = yr; else if (ny == 2) y2 = yr; else if (ny == 3) y3 = yr;
;                     else {
; #pragma unroll
;                         for (int i = 0; i < 8; ++i) { const u32x2 w = *(const u32x2*)(yr + i * 256 + lane * 4);
;                             cacc[i * 4] += bflo(w[0]); cacc[i * 4 + 1] += bfhi(w[0]); cacc[i * 4 + 2] += bflo(w[1]); cacc[i * 4 + 3] += bfhi(w[1]); }
;                     }
;                     ++ny;
;                 }
;             }
.LBB0_1833:
	s_or_b64 exec, exec, s[28:29]
	v_add_u32_e32 v88, 1, v88
	s_or_b64 exec, exec, s[16:17]
	v_cmp_lt_i32_e32 vcc, v1, v78
	s_and_saveexec_b64 s[16:17], vcc
	s_cbranch_execnz .LBB0_1739
.LBB0_1834:
	s_or_b64 exec, exec, s[16:17]
	v_cmp_lt_i32_e32 vcc, v86, v78
	s_and_saveexec_b64 s[16:17], vcc
	s_cbranch_execz .LBB0_1754

; DEVI float bflo(unsigned w) { return __uint_as_float(w << 16); }
; DEVI float bfhi(unsigned w) { return __uint_as_float(w & 0xffff0000u); }
; template <int MODE>
; DEVI void phase_rows(const Params& p, int l, char* smem) {
;     ...
;             for (int e = 0; e < 16; ++e) {
;                 const int r = rke[e];
;                 if (r < cap) {
;                     const int slot = lat ? (b * 256 + r) : (1024 + b * 32 + r);
;                     const bf16_t* yr = ydn + ((size_t)e * MSLOT + slot) * DM;
;                     if (ny == 0) y0 = yr; else if (ny == 1) y1 = yr; else if (ny == 2) y2 = yr; else if (ny == 3) y3 = yr;
;                     else {
; #pragma unroll
;                         for (int i = 0; i < 8; ++i) { const u32x2 w = *(const u32x2*)(yr + i * 256 + lane * 4);
;                             cacc[i * 4] += bflo(w[0]); cacc[i * 4 + 1] += bfhi(w[0]); cacc[i * 4 + 2] += bflo(w[1]); cacc[i * 4 + 3] += bfhi(w[1]); }
;                     }
;                     ++ny;
;                 }
;             }
.LBB0_1849:
	s_or_b64 exec, exec, s[28:29]
	v_add_u32_e32 v88, 1, v88
	s_or_b64 exec, exec, s[16:17]
	v_cmp_lt_i32_e32 vcc, v85, v78
	s_and_saveexec_b64 s[16:17], vcc
	s_cbranch_execnz .LBB0_1755
.LBB0_1850:
	s_or_b64 exec, exec, s[16:17]
	v_cmp_lt_i32_e32 vcc, v84, v78
	s_and_saveexec_b64 s[16:17], vcc
	s_cbranch_execz .LBB0_1770

; DEVI float bflo(unsigned w) { return __uint_as_float(w << 16); }
; DEVI float bfhi(unsigned w) { return __uint_as_float(w & 0xffff0000u); }
; template <int MODE>
; DEVI void phase_rows(const Params& p, int l, char* smem) {
;     ...
;             for (int e = 0; e < 16; ++e) {
;                 const int r = rke[e];
;                 if (r < cap) {
;                     const int slot = lat ? (b * 256 + r) : (1024 + b * 32 + r);
;                     const bf16_t* yr = ydn + ((size_t)e * MSLOT + slot) * DM;
;                     if (ny == 0) y0 = yr; else if (ny == 1) y1 = yr; else if (ny == 2) y2 = yr; else if (ny == 3) y3 = yr;
;                     else {
; #pragma unroll
;                         for (int i = 0; i < 8; ++i) { const u32x2 w = *(const u32x2*)(yr + i * 256 + lane * 4);
;                             cacc[i * 4] += bflo(w[0]); cacc[i * 4 + 1] += bfhi(w[0]); cacc[i * 4 + 2] += bflo(w[1]); cacc[i * 4 + 3] += bfhi(w[1]); }
;                     }
;                     ++ny;
;                 }
;             }
.LBB0_1865:
	s_or_b64 exec, exec, s[28:29]
	v_add_u32_e32 v88, 1, v88
	s_or_b64 exec, exec, s[16:17]
	v_cmp_lt_i32_e32 vcc, v83, v78
	s_and_saveexec_b64 s[16:17], vcc
	s_cbranch_execnz .LBB0_1771
.LBB0_1866:
	s_or_b64 exec, exec, s[16:17]
	v_cmp_lt_i32_e32 vcc, v82, v78
	s_and_saveexec_b64 s[16:17], vcc
	s_cbranch_execz .LBB0_1786

; DEVI float bflo(unsigned w) { return __uint_as_float(w << 16); }
; DEVI float bfhi(unsigned w) { return __uint_as_float(w & 0xffff0000u); }
; template <int MODE>
; DEVI void phase_rows(const Params& p, int l, char* smem) {
;     ...
;             for (int e = 0; e < 16; ++e) {
;                 const int r = rke[e];
;                 if (r < cap) {
;                     const int slot = lat ? (b * 256 + r) : (1024 + b * 32 + r);
;                     const bf16_t* yr = ydn + ((size_t)e * MSLOT + slot) * DM;
;                     if (ny == 0) y0 = yr; else if (ny == 1) y1 = yr; else if (ny == 2) y2 = yr; else if (ny == 3) y3 = yr;
;                     else {
; #pragma unroll
;                         for (int i = 0; i < 8; ++i) { const u32x2 w = *(const u32x2*)(yr + i * 256 + lane * 4);
;                             cacc[i * 4] += bflo(w[0]); cacc[i * 4 + 1] += bfhi(w[0]); cacc[i * 4 + 2] += bflo(w[1]); cacc[i * 4 + 3] += bfhi(w[1]); }
;                     }
;                     ++ny;
;                 }
;             }
.LBB0_1881:
	s_or_b64 exec, exec, s[28:29]
	v_add_u32_e32 v88, 1, v88
	s_or_b64 exec, exec, s[16:17]
	v_cmp_lt_i32_e32 vcc, v81, v78
	s_and_saveexec_b64 s[16:17], vcc
	s_cbranch_execnz .LBB0_1787
.LBB0_1882:
	s_or_b64 exec, exec, s[16:17]
	v_cmp_lt_i32_e32 vcc, v79, v78
	s_and_saveexec_b64 s[16:17], vcc
	s_cbranch_execz .LBB0_1683
